# P6 chained-GEMM epilogue re-emitted with unorm8 gate loads batched (16 in flight) on top of v28
# speedup vs baseline: 1.0273x; 1.0052x over previous
.LBB0_1496:
	s_cmpk_gt_i32 s34, 0xff
	s_cselect_b64 s[36:37], -1, 0
	s_lshl_b32 s7, s34, 8
	s_lshl_b32 s6, s6, 8
	s_add_i32 s25, s7, 0xffff0000
	s_add_i32 s27, s6, 0xfffffc00
	s_cmpk_lt_i32 s34, 0x100
	s_cselect_b32 s7, s7, s25
	v_add_u32_e32 v150, s7, v1
	s_cselect_b32 s6, s6, s27
	v_ashrrev_i32_e32 v151, 31, v150
	v_or_b32_e32 v4, s6, v157
	v_lshlrev_b64 v[154:155], 11, v[150:151]
	v_lshl_add_u64 v[152:153], s[76:77], 0, v[154:155]
	v_ashrrev_i32_e32 v5, 31, v4
	v_lshl_add_u64 v[152:153], v[152:153], 0, v[4:5]
	v_lshl_add_u64 v[154:155], s[8:9], 0, v[154:155]
	v_lshl_add_u64 v[154:155], v[4:5], 1, v[154:155]
	v_mov_b32_e32 v176, v152
	v_mov_b32_e32 v177, v153
	v_mov_b32_e32 v174, v154
	v_mov_b32_e32 v175, v155
	s_and_b64 vcc, exec, s[36:37]
	s_cbranch_vccnz .Lp6_second
	global_load_dwordx2 v[178:179], v[176:177], off offset:1024
	global_load_dwordx2 v[180:181], v[176:177], off
	global_load_dwordx2 v[182:183], v[176:177], off offset:1152
	global_load_dwordx2 v[184:185], v[176:177], off offset:128
	v_add_co_u32_e32 v176, vcc, 0x8000, v176
	s_nop 1
	v_addc_co_u32_e32 v177, vcc, 0, v177, vcc
	global_load_dwordx2 v[186:187], v[176:177], off offset:1024
	global_load_dwordx2 v[188:189], v[176:177], off
	global_load_dwordx2 v[190:191], v[176:177], off offset:1152
	global_load_dwordx2 v[192:193], v[176:177], off offset:128
	v_add_co_u32_e32 v176, vcc, 0x8000, v176
	s_nop 1
	v_addc_co_u32_e32 v177, vcc, 0, v177, vcc
	global_load_dwordx2 v[194:195], v[176:177], off offset:1024
	global_load_dwordx2 v[196:197], v[176:177], off
	global_load_dwordx2 v[198:199], v[176:177], off offset:1152
	global_load_dwordx2 v[202:203], v[176:177], off offset:128
	v_add_co_u32_e32 v176, vcc, 0x8000, v176
	s_nop 1
	v_addc_co_u32_e32 v177, vcc, 0, v177, vcc
	global_load_dwordx2 v[204:205], v[176:177], off offset:1024
	global_load_dwordx2 v[206:207], v[176:177], off
	global_load_dwordx2 v[208:209], v[176:177], off offset:1152
	global_load_dwordx2 v[210:211], v[176:177], off offset:128
	s_waitcnt vmcnt(14)
	v_cvt_f32_ubyte0_e32 v160, v178
	v_cvt_f32_ubyte1_e32 v161, v178
	v_cvt_f32_ubyte2_e32 v162, v178
	v_cvt_f32_ubyte3_e32 v163, v178
	v_cvt_f32_ubyte0_e32 v164, v179
	v_cvt_f32_ubyte1_e32 v165, v179
	v_cvt_f32_ubyte2_e32 v166, v179
	v_cvt_f32_ubyte3_e32 v167, v179
	v_mul_f32_e32 v160, 0x3b808081, v160
	v_mul_f32_e32 v161, 0x3b808081, v161
	v_mul_f32_e32 v162, 0x3b808081, v162
	v_mul_f32_e32 v163, 0x3b808081, v163
	v_mul_f32_e32 v164, 0x3b808081, v164
	v_mul_f32_e32 v165, 0x3b808081, v165
	v_mul_f32_e32 v166, 0x3b808081, v166
	v_mul_f32_e32 v167, 0x3b808081, v167
	v_max_f32_e32 v160, 0xda24260, v160
	v_max_f32_e32 v161, 0xda24260, v161
	v_max_f32_e32 v162, 0xda24260, v162
	v_max_f32_e32 v163, 0xda24260, v163
	v_max_f32_e32 v164, 0xda24260, v164
	v_max_f32_e32 v165, 0xda24260, v165
	v_max_f32_e32 v166, 0xda24260, v166
	v_max_f32_e32 v167, 0xda24260, v167
	v_rcp_f32_e32 v160, v160
	v_rcp_f32_e32 v161, v161
	v_rcp_f32_e32 v162, v162
	v_rcp_f32_e32 v163, v163
	v_rcp_f32_e32 v164, v164
	v_rcp_f32_e32 v165, v165
	v_rcp_f32_e32 v166, v166
	v_rcp_f32_e32 v167, v167
	v_cvt_f32_ubyte0_e32 v168, v180
	v_cvt_f32_ubyte1_e32 v169, v180
	v_cvt_f32_ubyte2_e32 v170, v180
	v_cvt_f32_ubyte3_e32 v171, v180
	v_cvt_f32_ubyte0_e32 v172, v181
	v_cvt_f32_ubyte1_e32 v173, v181
	v_cvt_f32_ubyte2_e32 v174, v181
	v_cvt_f32_ubyte3_e32 v175, v181
	v_mul_f32_e32 v168, 0x3b808081, v168
	v_mul_f32_e32 v169, 0x3b808081, v169
	v_mul_f32_e32 v170, 0x3b808081, v170
	v_mul_f32_e32 v171, 0x3b808081, v171
	v_mul_f32_e32 v172, 0x3b808081, v172
	v_mul_f32_e32 v173, 0x3b808081, v173
	v_mul_f32_e32 v174, 0x3b808081, v174
	v_mul_f32_e32 v175, 0x3b808081, v175
	v_mul_f32_e32 v168, v160, v168
	v_mul_f32_e32 v169, v161, v169
	v_mul_f32_e32 v170, v162, v170
	v_mul_f32_e32 v171, v163, v171
	v_mul_f32_e32 v172, v164, v172
	v_mul_f32_e32 v173, v165, v173
	v_mul_f32_e32 v174, v166, v174
	v_mul_f32_e32 v175, v167, v175
	v_mul_f32_e32 v130, v130, v168
	v_mul_f32_e32 v131, v131, v169
	v_mul_f32_e32 v132, v132, v170
	v_mul_f32_e32 v133, v133, v171
	v_mul_f32_e32 v126, v126, v172
	v_mul_f32_e32 v127, v127, v173
	v_mul_f32_e32 v128, v128, v174
	v_mul_f32_e32 v129, v129, v175
	v_add_co_u32_e32 v176, vcc, 0x28000, v176
	s_nop 1
	v_addc_co_u32_e32 v177, vcc, 0, v177, vcc
	global_load_dwordx2 v[178:179], v[176:177], off offset:1024
	global_load_dwordx2 v[180:181], v[176:177], off
	s_waitcnt vmcnt(14)
	v_cvt_f32_ubyte0_e32 v160, v182
	v_cvt_f32_ubyte1_e32 v161, v182
	v_cvt_f32_ubyte2_e32 v162, v182
	v_cvt_f32_ubyte3_e32 v163, v182
	v_cvt_f32_ubyte0_e32 v164, v183
	v_cvt_f32_ubyte1_e32 v165, v183
	v_cvt_f32_ubyte2_e32 v166, v183
	v_cvt_f32_ubyte3_e32 v167, v183
	v_mul_f32_e32 v160, 0x3b808081, v160
	v_mul_f32_e32 v161, 0x3b808081, v161
	v_mul_f32_e32 v162, 0x3b808081, v162
	v_mul_f32_e32 v163, 0x3b808081, v163
	v_mul_f32_e32 v164, 0x3b808081, v164
	v_mul_f32_e32 v165, 0x3b808081, v165
	v_mul_f32_e32 v166, 0x3b808081, v166
	v_mul_f32_e32 v167, 0x3b808081, v167
	v_max_f32_e32 v160, 0xda24260, v160
	v_max_f32_e32 v161, 0xda24260, v161
	v_max_f32_e32 v162, 0xda24260, v162
	v_max_f32_e32 v163, 0xda24260, v163
	v_max_f32_e32 v164, 0xda24260, v164
	v_max_f32_e32 v165, 0xda24260, v165
	v_max_f32_e32 v166, 0xda24260, v166
	v_max_f32_e32 v167, 0xda24260, v167
	v_rcp_f32_e32 v160, v160
	v_rcp_f32_e32 v161, v161
	v_rcp_f32_e32 v162, v162
	v_rcp_f32_e32 v163, v163
	v_rcp_f32_e32 v164, v164
	v_rcp_f32_e32 v165, v165
	v_rcp_f32_e32 v166, v166
	v_rcp_f32_e32 v167, v167
	v_cvt_f32_ubyte0_e32 v168, v184
	v_cvt_f32_ubyte1_e32 v169, v184
	v_cvt_f32_ubyte2_e32 v170, v184
	v_cvt_f32_ubyte3_e32 v171, v184
	v_cvt_f32_ubyte0_e32 v172, v185
	v_cvt_f32_ubyte1_e32 v173, v185
	v_cvt_f32_ubyte2_e32 v174, v185
	v_cvt_f32_ubyte3_e32 v175, v185
	v_mul_f32_e32 v168, 0x3b808081, v168
	v_mul_f32_e32 v169, 0x3b808081, v169
	v_mul_f32_e32 v170, 0x3b808081, v170
	v_mul_f32_e32 v171, 0x3b808081, v171
	v_mul_f32_e32 v172, 0x3b808081, v172
	v_mul_f32_e32 v173, 0x3b808081, v173
	v_mul_f32_e32 v174, 0x3b808081, v174
	v_mul_f32_e32 v175, 0x3b808081, v175
	v_mul_f32_e32 v168, v160, v168
	v_mul_f32_e32 v169, v161, v169
	v_mul_f32_e32 v170, v162, v170
	v_mul_f32_e32 v171, v163, v171
	v_mul_f32_e32 v172, v164, v172
	v_mul_f32_e32 v173, v165, v173
	v_mul_f32_e32 v174, v166, v174
	v_mul_f32_e32 v175, v167, v175
	v_mul_f32_e32 v98, v98, v168
	v_mul_f32_e32 v99, v99, v169
	v_mul_f32_e32 v100, v100, v170
	v_mul_f32_e32 v101, v101, v171
	v_mul_f32_e32 v94, v94, v172
	v_mul_f32_e32 v95, v95, v173
	v_mul_f32_e32 v96, v96, v174
	v_mul_f32_e32 v97, v97, v175
	global_load_dwordx2 v[182:183], v[176:177], off offset:1152
	global_load_dwordx2 v[184:185], v[176:177], off offset:128
	s_waitcnt vmcnt(14)
	v_cvt_f32_ubyte0_e32 v160, v186
	v_cvt_f32_ubyte1_e32 v161, v186
	v_cvt_f32_ubyte2_e32 v162, v186
	v_cvt_f32_ubyte3_e32 v163, v186
	v_cvt_f32_ubyte0_e32 v164, v187
	v_cvt_f32_ubyte1_e32 v165, v187
	v_cvt_f32_ubyte2_e32 v166, v187
	v_cvt_f32_ubyte3_e32 v167, v187
	v_mul_f32_e32 v160, 0x3b808081, v160
	v_mul_f32_e32 v161, 0x3b808081, v161
	v_mul_f32_e32 v162, 0x3b808081, v162
	v_mul_f32_e32 v163, 0x3b808081, v163
	v_mul_f32_e32 v164, 0x3b808081, v164
	v_mul_f32_e32 v165, 0x3b808081, v165
	v_mul_f32_e32 v166, 0x3b808081, v166
	v_mul_f32_e32 v167, 0x3b808081, v167
	v_max_f32_e32 v160, 0xda24260, v160
	v_max_f32_e32 v161, 0xda24260, v161
	v_max_f32_e32 v162, 0xda24260, v162
	v_max_f32_e32 v163, 0xda24260, v163
	v_max_f32_e32 v164, 0xda24260, v164
	v_max_f32_e32 v165, 0xda24260, v165
	v_max_f32_e32 v166, 0xda24260, v166
	v_max_f32_e32 v167, 0xda24260, v167
	v_rcp_f32_e32 v160, v160
	v_rcp_f32_e32 v161, v161
	v_rcp_f32_e32 v162, v162
	v_rcp_f32_e32 v163, v163
	v_rcp_f32_e32 v164, v164
	v_rcp_f32_e32 v165, v165
	v_rcp_f32_e32 v166, v166
	v_rcp_f32_e32 v167, v167
	v_cvt_f32_ubyte0_e32 v168, v188
	v_cvt_f32_ubyte1_e32 v169, v188
	v_cvt_f32_ubyte2_e32 v170, v188
	v_cvt_f32_ubyte3_e32 v171, v188
	v_cvt_f32_ubyte0_e32 v172, v189
	v_cvt_f32_ubyte1_e32 v173, v189
	v_cvt_f32_ubyte2_e32 v174, v189
	v_cvt_f32_ubyte3_e32 v175, v189
	v_mul_f32_e32 v168, 0x3b808081, v168
	v_mul_f32_e32 v169, 0x3b808081, v169
	v_mul_f32_e32 v170, 0x3b808081, v170
	v_mul_f32_e32 v171, 0x3b808081, v171
	v_mul_f32_e32 v172, 0x3b808081, v172
	v_mul_f32_e32 v173, 0x3b808081, v173
	v_mul_f32_e32 v174, 0x3b808081, v174
	v_mul_f32_e32 v175, 0x3b808081, v175
	v_mul_f32_e32 v168, v160, v168
	v_mul_f32_e32 v169, v161, v169
	v_mul_f32_e32 v170, v162, v170
	v_mul_f32_e32 v171, v163, v171
	v_mul_f32_e32 v172, v164, v172
	v_mul_f32_e32 v173, v165, v173
	v_mul_f32_e32 v174, v166, v174
	v_mul_f32_e32 v175, v167, v175
	v_mul_f32_e32 v122, v122, v168
	v_mul_f32_e32 v123, v123, v169
	v_mul_f32_e32 v124, v124, v170
	v_mul_f32_e32 v125, v125, v171
	v_mul_f32_e32 v118, v118, v172
	v_mul_f32_e32 v119, v119, v173
	v_mul_f32_e32 v120, v120, v174
	v_mul_f32_e32 v121, v121, v175
	v_add_co_u32_e32 v176, vcc, 0x8000, v176
	s_nop 1
	v_addc_co_u32_e32 v177, vcc, 0, v177, vcc
	global_load_dwordx2 v[186:187], v[176:177], off offset:1024
	global_load_dwordx2 v[188:189], v[176:177], off
	s_waitcnt vmcnt(14)
	v_cvt_f32_ubyte0_e32 v160, v190
	v_cvt_f32_ubyte1_e32 v161, v190
	v_cvt_f32_ubyte2_e32 v162, v190
	v_cvt_f32_ubyte3_e32 v163, v190
	v_cvt_f32_ubyte0_e32 v164, v191
	v_cvt_f32_ubyte1_e32 v165, v191
	v_cvt_f32_ubyte2_e32 v166, v191
	v_cvt_f32_ubyte3_e32 v167, v191
	v_mul_f32_e32 v160, 0x3b808081, v160
	v_mul_f32_e32 v161, 0x3b808081, v161
	v_mul_f32_e32 v162, 0x3b808081, v162
	v_mul_f32_e32 v163, 0x3b808081, v163
	v_mul_f32_e32 v164, 0x3b808081, v164
	v_mul_f32_e32 v165, 0x3b808081, v165
	v_mul_f32_e32 v166, 0x3b808081, v166
	v_mul_f32_e32 v167, 0x3b808081, v167
	v_max_f32_e32 v160, 0xda24260, v160
	v_max_f32_e32 v161, 0xda24260, v161
	v_max_f32_e32 v162, 0xda24260, v162
	v_max_f32_e32 v163, 0xda24260, v163
	v_max_f32_e32 v164, 0xda24260, v164
	v_max_f32_e32 v165, 0xda24260, v165
	v_max_f32_e32 v166, 0xda24260, v166
	v_max_f32_e32 v167, 0xda24260, v167
	v_rcp_f32_e32 v160, v160
	v_rcp_f32_e32 v161, v161
	v_rcp_f32_e32 v162, v162
	v_rcp_f32_e32 v163, v163
	v_rcp_f32_e32 v164, v164
	v_rcp_f32_e32 v165, v165
	v_rcp_f32_e32 v166, v166
	v_rcp_f32_e32 v167, v167
	v_cvt_f32_ubyte0_e32 v168, v192
	v_cvt_f32_ubyte1_e32 v169, v192
	v_cvt_f32_ubyte2_e32 v170, v192
	v_cvt_f32_ubyte3_e32 v171, v192
	v_cvt_f32_ubyte0_e32 v172, v193
	v_cvt_f32_ubyte1_e32 v173, v193
	v_cvt_f32_ubyte2_e32 v174, v193
	v_cvt_f32_ubyte3_e32 v175, v193
	v_mul_f32_e32 v168, 0x3b808081, v168
	v_mul_f32_e32 v169, 0x3b808081, v169
	v_mul_f32_e32 v170, 0x3b808081, v170
	v_mul_f32_e32 v171, 0x3b808081, v171
	v_mul_f32_e32 v172, 0x3b808081, v172
	v_mul_f32_e32 v173, 0x3b808081, v173
	v_mul_f32_e32 v174, 0x3b808081, v174
	v_mul_f32_e32 v175, 0x3b808081, v175
	v_mul_f32_e32 v168, v160, v168
	v_mul_f32_e32 v169, v161, v169
	v_mul_f32_e32 v170, v162, v170
	v_mul_f32_e32 v171, v163, v171
	v_mul_f32_e32 v172, v164, v172
	v_mul_f32_e32 v173, v165, v173
	v_mul_f32_e32 v174, v166, v174
	v_mul_f32_e32 v175, v167, v175
	v_mul_f32_e32 v90, v90, v168
	v_mul_f32_e32 v91, v91, v169
	v_mul_f32_e32 v92, v92, v170
	v_mul_f32_e32 v93, v93, v171
	v_mul_f32_e32 v86, v86, v172
	v_mul_f32_e32 v87, v87, v173
	v_mul_f32_e32 v88, v88, v174
	v_mul_f32_e32 v89, v89, v175
	global_load_dwordx2 v[190:191], v[176:177], off offset:1152
	global_load_dwordx2 v[192:193], v[176:177], off offset:128
	s_waitcnt vmcnt(14)
	v_cvt_f32_ubyte0_e32 v160, v194
	v_cvt_f32_ubyte1_e32 v161, v194
	v_cvt_f32_ubyte2_e32 v162, v194
	v_cvt_f32_ubyte3_e32 v163, v194
	v_cvt_f32_ubyte0_e32 v164, v195
	v_cvt_f32_ubyte1_e32 v165, v195
	v_cvt_f32_ubyte2_e32 v166, v195
	v_cvt_f32_ubyte3_e32 v167, v195
	v_mul_f32_e32 v160, 0x3b808081, v160
	v_mul_f32_e32 v161, 0x3b808081, v161
	v_mul_f32_e32 v162, 0x3b808081, v162
	v_mul_f32_e32 v163, 0x3b808081, v163
	v_mul_f32_e32 v164, 0x3b808081, v164
	v_mul_f32_e32 v165, 0x3b808081, v165
	v_mul_f32_e32 v166, 0x3b808081, v166
	v_mul_f32_e32 v167, 0x3b808081, v167
	v_max_f32_e32 v160, 0xda24260, v160
	v_max_f32_e32 v161, 0xda24260, v161
	v_max_f32_e32 v162, 0xda24260, v162
	v_max_f32_e32 v163, 0xda24260, v163
	v_max_f32_e32 v164, 0xda24260, v164
	v_max_f32_e32 v165, 0xda24260, v165
	v_max_f32_e32 v166, 0xda24260, v166
	v_max_f32_e32 v167, 0xda24260, v167
	v_rcp_f32_e32 v160, v160
	v_rcp_f32_e32 v161, v161
	v_rcp_f32_e32 v162, v162
	v_rcp_f32_e32 v163, v163
	v_rcp_f32_e32 v164, v164
	v_rcp_f32_e32 v165, v165
	v_rcp_f32_e32 v166, v166
	v_rcp_f32_e32 v167, v167
	v_cvt_f32_ubyte0_e32 v168, v196
	v_cvt_f32_ubyte1_e32 v169, v196
	v_cvt_f32_ubyte2_e32 v170, v196
	v_cvt_f32_ubyte3_e32 v171, v196
	v_cvt_f32_ubyte0_e32 v172, v197
	v_cvt_f32_ubyte1_e32 v173, v197
	v_cvt_f32_ubyte2_e32 v174, v197
	v_cvt_f32_ubyte3_e32 v175, v197
	v_mul_f32_e32 v168, 0x3b808081, v168
	v_mul_f32_e32 v169, 0x3b808081, v169
	v_mul_f32_e32 v170, 0x3b808081, v170
	v_mul_f32_e32 v171, 0x3b808081, v171
	v_mul_f32_e32 v172, 0x3b808081, v172
	v_mul_f32_e32 v173, 0x3b808081, v173
	v_mul_f32_e32 v174, 0x3b808081, v174
	v_mul_f32_e32 v175, 0x3b808081, v175
	v_mul_f32_e32 v168, v160, v168
	v_mul_f32_e32 v169, v161, v169
	v_mul_f32_e32 v170, v162, v170
	v_mul_f32_e32 v171, v163, v171
	v_mul_f32_e32 v172, v164, v172
	v_mul_f32_e32 v173, v165, v173
	v_mul_f32_e32 v174, v166, v174
	v_mul_f32_e32 v175, v167, v175
	v_mul_f32_e32 v114, v114, v168
	v_mul_f32_e32 v115, v115, v169
	v_mul_f32_e32 v116, v116, v170
	v_mul_f32_e32 v117, v117, v171
	v_mul_f32_e32 v110, v110, v172
	v_mul_f32_e32 v111, v111, v173
	v_mul_f32_e32 v112, v112, v174
	v_mul_f32_e32 v113, v113, v175
	v_add_co_u32_e32 v176, vcc, 0x8000, v176
	s_nop 1
	v_addc_co_u32_e32 v177, vcc, 0, v177, vcc
	global_load_dwordx2 v[194:195], v[176:177], off offset:1024
	global_load_dwordx2 v[196:197], v[176:177], off
	s_waitcnt vmcnt(14)
	v_cvt_f32_ubyte0_e32 v160, v198
	v_cvt_f32_ubyte1_e32 v161, v198
	v_cvt_f32_ubyte2_e32 v162, v198
	v_cvt_f32_ubyte3_e32 v163, v198
	v_cvt_f32_ubyte0_e32 v164, v199
	v_cvt_f32_ubyte1_e32 v165, v199
	v_cvt_f32_ubyte2_e32 v166, v199
	v_cvt_f32_ubyte3_e32 v167, v199
	v_mul_f32_e32 v160, 0x3b808081, v160
	v_mul_f32_e32 v161, 0x3b808081, v161
	v_mul_f32_e32 v162, 0x3b808081, v162
	v_mul_f32_e32 v163, 0x3b808081, v163
	v_mul_f32_e32 v164, 0x3b808081, v164
	v_mul_f32_e32 v165, 0x3b808081, v165
	v_mul_f32_e32 v166, 0x3b808081, v166
	v_mul_f32_e32 v167, 0x3b808081, v167
	v_max_f32_e32 v160, 0xda24260, v160
	v_max_f32_e32 v161, 0xda24260, v161
	v_max_f32_e32 v162, 0xda24260, v162
	v_max_f32_e32 v163, 0xda24260, v163
	v_max_f32_e32 v164, 0xda24260, v164
	v_max_f32_e32 v165, 0xda24260, v165
	v_max_f32_e32 v166, 0xda24260, v166
	v_max_f32_e32 v167, 0xda24260, v167
	v_rcp_f32_e32 v160, v160
	v_rcp_f32_e32 v161, v161
	v_rcp_f32_e32 v162, v162
	v_rcp_f32_e32 v163, v163
	v_rcp_f32_e32 v164, v164
	v_rcp_f32_e32 v165, v165
	v_rcp_f32_e32 v166, v166
	v_rcp_f32_e32 v167, v167
	v_cvt_f32_ubyte0_e32 v168, v202
	v_cvt_f32_ubyte1_e32 v169, v202
	v_cvt_f32_ubyte2_e32 v170, v202
	v_cvt_f32_ubyte3_e32 v171, v202
	v_cvt_f32_ubyte0_e32 v172, v203
	v_cvt_f32_ubyte1_e32 v173, v203
	v_cvt_f32_ubyte2_e32 v174, v203
	v_cvt_f32_ubyte3_e32 v175, v203
	v_mul_f32_e32 v168, 0x3b808081, v168
	v_mul_f32_e32 v169, 0x3b808081, v169
	v_mul_f32_e32 v170, 0x3b808081, v170
	v_mul_f32_e32 v171, 0x3b808081, v171
	v_mul_f32_e32 v172, 0x3b808081, v172
	v_mul_f32_e32 v173, 0x3b808081, v173
	v_mul_f32_e32 v174, 0x3b808081, v174
	v_mul_f32_e32 v175, 0x3b808081, v175
	v_mul_f32_e32 v168, v160, v168
	v_mul_f32_e32 v169, v161, v169
	v_mul_f32_e32 v170, v162, v170
	v_mul_f32_e32 v171, v163, v171
	v_mul_f32_e32 v172, v164, v172
	v_mul_f32_e32 v173, v165, v173
	v_mul_f32_e32 v174, v166, v174
	v_mul_f32_e32 v175, v167, v175
	v_mul_f32_e32 v82, v82, v168
	v_mul_f32_e32 v83, v83, v169
	v_mul_f32_e32 v84, v84, v170
	v_mul_f32_e32 v85, v85, v171
	v_mul_f32_e32 v78, v78, v172
	v_mul_f32_e32 v79, v79, v173
	v_mul_f32_e32 v80, v80, v174
	v_mul_f32_e32 v81, v81, v175
	global_load_dwordx2 v[198:199], v[176:177], off offset:1152
	global_load_dwordx2 v[202:203], v[176:177], off offset:128
	s_waitcnt vmcnt(14)
	v_cvt_f32_ubyte0_e32 v160, v204
	v_cvt_f32_ubyte1_e32 v161, v204
	v_cvt_f32_ubyte2_e32 v162, v204
	v_cvt_f32_ubyte3_e32 v163, v204
	v_cvt_f32_ubyte0_e32 v164, v205
	v_cvt_f32_ubyte1_e32 v165, v205
	v_cvt_f32_ubyte2_e32 v166, v205
	v_cvt_f32_ubyte3_e32 v167, v205
	v_mul_f32_e32 v160, 0x3b808081, v160
	v_mul_f32_e32 v161, 0x3b808081, v161
	v_mul_f32_e32 v162, 0x3b808081, v162
	v_mul_f32_e32 v163, 0x3b808081, v163
	v_mul_f32_e32 v164, 0x3b808081, v164
	v_mul_f32_e32 v165, 0x3b808081, v165
	v_mul_f32_e32 v166, 0x3b808081, v166
	v_mul_f32_e32 v167, 0x3b808081, v167
	v_max_f32_e32 v160, 0xda24260, v160
	v_max_f32_e32 v161, 0xda24260, v161
	v_max_f32_e32 v162, 0xda24260, v162
	v_max_f32_e32 v163, 0xda24260, v163
	v_max_f32_e32 v164, 0xda24260, v164
	v_max_f32_e32 v165, 0xda24260, v165
	v_max_f32_e32 v166, 0xda24260, v166
	v_max_f32_e32 v167, 0xda24260, v167
	v_rcp_f32_e32 v160, v160
	v_rcp_f32_e32 v161, v161
	v_rcp_f32_e32 v162, v162
	v_rcp_f32_e32 v163, v163
	v_rcp_f32_e32 v164, v164
	v_rcp_f32_e32 v165, v165
	v_rcp_f32_e32 v166, v166
	v_rcp_f32_e32 v167, v167
	v_cvt_f32_ubyte0_e32 v168, v206
	v_cvt_f32_ubyte1_e32 v169, v206
	v_cvt_f32_ubyte2_e32 v170, v206
	v_cvt_f32_ubyte3_e32 v171, v206
	v_cvt_f32_ubyte0_e32 v172, v207
	v_cvt_f32_ubyte1_e32 v173, v207
	v_cvt_f32_ubyte2_e32 v174, v207
	v_cvt_f32_ubyte3_e32 v175, v207
	v_mul_f32_e32 v168, 0x3b808081, v168
	v_mul_f32_e32 v169, 0x3b808081, v169
	v_mul_f32_e32 v170, 0x3b808081, v170
	v_mul_f32_e32 v171, 0x3b808081, v171
	v_mul_f32_e32 v172, 0x3b808081, v172
	v_mul_f32_e32 v173, 0x3b808081, v173
	v_mul_f32_e32 v174, 0x3b808081, v174
	v_mul_f32_e32 v175, 0x3b808081, v175
	v_mul_f32_e32 v168, v160, v168
	v_mul_f32_e32 v169, v161, v169
	v_mul_f32_e32 v170, v162, v170
	v_mul_f32_e32 v171, v163, v171
	v_mul_f32_e32 v172, v164, v172
	v_mul_f32_e32 v173, v165, v173
	v_mul_f32_e32 v174, v166, v174
	v_mul_f32_e32 v175, v167, v175
	v_mul_f32_e32 v106, v106, v168
	v_mul_f32_e32 v107, v107, v169
	v_mul_f32_e32 v108, v108, v170
	v_mul_f32_e32 v109, v109, v171
	v_mul_f32_e32 v102, v102, v172
	v_mul_f32_e32 v103, v103, v173
	v_mul_f32_e32 v104, v104, v174
	v_mul_f32_e32 v105, v105, v175
	v_add_co_u32_e32 v176, vcc, 0x8000, v176
	s_nop 1
	v_addc_co_u32_e32 v177, vcc, 0, v177, vcc
	global_load_dwordx2 v[204:205], v[176:177], off offset:1024
	global_load_dwordx2 v[206:207], v[176:177], off
	s_waitcnt vmcnt(14)
	v_cvt_f32_ubyte0_e32 v160, v208
	v_cvt_f32_ubyte1_e32 v161, v208
	v_cvt_f32_ubyte2_e32 v162, v208
	v_cvt_f32_ubyte3_e32 v163, v208
	v_cvt_f32_ubyte0_e32 v164, v209
	v_cvt_f32_ubyte1_e32 v165, v209
	v_cvt_f32_ubyte2_e32 v166, v209
	v_cvt_f32_ubyte3_e32 v167, v209
	v_mul_f32_e32 v160, 0x3b808081, v160
	v_mul_f32_e32 v161, 0x3b808081, v161
	v_mul_f32_e32 v162, 0x3b808081, v162
	v_mul_f32_e32 v163, 0x3b808081, v163
	v_mul_f32_e32 v164, 0x3b808081, v164
	v_mul_f32_e32 v165, 0x3b808081, v165
	v_mul_f32_e32 v166, 0x3b808081, v166
	v_mul_f32_e32 v167, 0x3b808081, v167
	v_max_f32_e32 v160, 0xda24260, v160
	v_max_f32_e32 v161, 0xda24260, v161
	v_max_f32_e32 v162, 0xda24260, v162
	v_max_f32_e32 v163, 0xda24260, v163
	v_max_f32_e32 v164, 0xda24260, v164
	v_max_f32_e32 v165, 0xda24260, v165
	v_max_f32_e32 v166, 0xda24260, v166
	v_max_f32_e32 v167, 0xda24260, v167
	v_rcp_f32_e32 v160, v160
	v_rcp_f32_e32 v161, v161
	v_rcp_f32_e32 v162, v162
	v_rcp_f32_e32 v163, v163
	v_rcp_f32_e32 v164, v164
	v_rcp_f32_e32 v165, v165
	v_rcp_f32_e32 v166, v166
	v_rcp_f32_e32 v167, v167
	v_cvt_f32_ubyte0_e32 v168, v210
	v_cvt_f32_ubyte1_e32 v169, v210
	v_cvt_f32_ubyte2_e32 v170, v210
	v_cvt_f32_ubyte3_e32 v171, v210
	v_cvt_f32_ubyte0_e32 v172, v211
	v_cvt_f32_ubyte1_e32 v173, v211
	v_cvt_f32_ubyte2_e32 v174, v211
	v_cvt_f32_ubyte3_e32 v175, v211
	v_mul_f32_e32 v168, 0x3b808081, v168
	v_mul_f32_e32 v169, 0x3b808081, v169
	v_mul_f32_e32 v170, 0x3b808081, v170
	v_mul_f32_e32 v171, 0x3b808081, v171
	v_mul_f32_e32 v172, 0x3b808081, v172
	v_mul_f32_e32 v173, 0x3b808081, v173
	v_mul_f32_e32 v174, 0x3b808081, v174
	v_mul_f32_e32 v175, 0x3b808081, v175
	v_mul_f32_e32 v168, v160, v168
	v_mul_f32_e32 v169, v161, v169
	v_mul_f32_e32 v170, v162, v170
	v_mul_f32_e32 v171, v163, v171
	v_mul_f32_e32 v172, v164, v172
	v_mul_f32_e32 v173, v165, v173
	v_mul_f32_e32 v174, v166, v174
	v_mul_f32_e32 v175, v167, v175
	v_mul_f32_e32 v74, v74, v168
	v_mul_f32_e32 v75, v75, v169
	v_mul_f32_e32 v76, v76, v170
	v_mul_f32_e32 v77, v77, v171
	v_mul_f32_e32 v70, v70, v172
	v_mul_f32_e32 v71, v71, v173
	v_mul_f32_e32 v72, v72, v174
	v_mul_f32_e32 v73, v73, v175
	global_load_dwordx2 v[208:209], v[176:177], off offset:1152
	global_load_dwordx2 v[210:211], v[176:177], off offset:128
	s_waitcnt vmcnt(14)
	v_cvt_f32_ubyte0_e32 v160, v178
	v_cvt_f32_ubyte1_e32 v161, v178
	v_cvt_f32_ubyte2_e32 v162, v178
	v_cvt_f32_ubyte3_e32 v163, v178
	v_cvt_f32_ubyte0_e32 v164, v179
	v_cvt_f32_ubyte1_e32 v165, v179
	v_cvt_f32_ubyte2_e32 v166, v179
	v_cvt_f32_ubyte3_e32 v167, v179
	v_mul_f32_e32 v160, 0x3b808081, v160
	v_mul_f32_e32 v161, 0x3b808081, v161
	v_mul_f32_e32 v162, 0x3b808081, v162
	v_mul_f32_e32 v163, 0x3b808081, v163
	v_mul_f32_e32 v164, 0x3b808081, v164
	v_mul_f32_e32 v165, 0x3b808081, v165
	v_mul_f32_e32 v166, 0x3b808081, v166
	v_mul_f32_e32 v167, 0x3b808081, v167
	v_max_f32_e32 v160, 0xda24260, v160
	v_max_f32_e32 v161, 0xda24260, v161
	v_max_f32_e32 v162, 0xda24260, v162
	v_max_f32_e32 v163, 0xda24260, v163
	v_max_f32_e32 v164, 0xda24260, v164
	v_max_f32_e32 v165, 0xda24260, v165
	v_max_f32_e32 v166, 0xda24260, v166
	v_max_f32_e32 v167, 0xda24260, v167
	v_rcp_f32_e32 v160, v160
	v_rcp_f32_e32 v161, v161
	v_rcp_f32_e32 v162, v162
	v_rcp_f32_e32 v163, v163
	v_rcp_f32_e32 v164, v164
	v_rcp_f32_e32 v165, v165
	v_rcp_f32_e32 v166, v166
	v_rcp_f32_e32 v167, v167
	v_cvt_f32_ubyte0_e32 v168, v180
	v_cvt_f32_ubyte1_e32 v169, v180
	v_cvt_f32_ubyte2_e32 v170, v180
	v_cvt_f32_ubyte3_e32 v171, v180
	v_cvt_f32_ubyte0_e32 v172, v181
	v_cvt_f32_ubyte1_e32 v173, v181
	v_cvt_f32_ubyte2_e32 v174, v181
	v_cvt_f32_ubyte3_e32 v175, v181
	v_mul_f32_e32 v168, 0x3b808081, v168
	v_mul_f32_e32 v169, 0x3b808081, v169
	v_mul_f32_e32 v170, 0x3b808081, v170
	v_mul_f32_e32 v171, 0x3b808081, v171
	v_mul_f32_e32 v172, 0x3b808081, v172
	v_mul_f32_e32 v173, 0x3b808081, v173
	v_mul_f32_e32 v174, 0x3b808081, v174
	v_mul_f32_e32 v175, 0x3b808081, v175
	v_mul_f32_e32 v168, v160, v168
	v_mul_f32_e32 v169, v161, v169
	v_mul_f32_e32 v170, v162, v170
	v_mul_f32_e32 v171, v163, v171
	v_mul_f32_e32 v172, v164, v172
	v_mul_f32_e32 v173, v165, v173
	v_mul_f32_e32 v174, v166, v174
	v_mul_f32_e32 v175, v167, v175
	v_mul_f32_e32 v66, v66, v168
	v_mul_f32_e32 v67, v67, v169
	v_mul_f32_e32 v68, v68, v170
	v_mul_f32_e32 v69, v69, v171
	v_mul_f32_e32 v62, v62, v172
	v_mul_f32_e32 v63, v63, v173
	v_mul_f32_e32 v64, v64, v174
	v_mul_f32_e32 v65, v65, v175
	s_waitcnt vmcnt(12)
	v_cvt_f32_ubyte0_e32 v160, v182
	v_cvt_f32_ubyte1_e32 v161, v182
	v_cvt_f32_ubyte2_e32 v162, v182
	v_cvt_f32_ubyte3_e32 v163, v182
	v_cvt_f32_ubyte0_e32 v164, v183
	v_cvt_f32_ubyte1_e32 v165, v183
	v_cvt_f32_ubyte2_e32 v166, v183
	v_cvt_f32_ubyte3_e32 v167, v183
	v_mul_f32_e32 v160, 0x3b808081, v160
	v_mul_f32_e32 v161, 0x3b808081, v161
	v_mul_f32_e32 v162, 0x3b808081, v162
	v_mul_f32_e32 v163, 0x3b808081, v163
	v_mul_f32_e32 v164, 0x3b808081, v164
	v_mul_f32_e32 v165, 0x3b808081, v165
	v_mul_f32_e32 v166, 0x3b808081, v166
	v_mul_f32_e32 v167, 0x3b808081, v167
	v_max_f32_e32 v160, 0xda24260, v160
	v_max_f32_e32 v161, 0xda24260, v161
	v_max_f32_e32 v162, 0xda24260, v162
	v_max_f32_e32 v163, 0xda24260, v163
	v_max_f32_e32 v164, 0xda24260, v164
	v_max_f32_e32 v165, 0xda24260, v165
	v_max_f32_e32 v166, 0xda24260, v166
	v_max_f32_e32 v167, 0xda24260, v167
	v_rcp_f32_e32 v160, v160
	v_rcp_f32_e32 v161, v161
	v_rcp_f32_e32 v162, v162
	v_rcp_f32_e32 v163, v163
	v_rcp_f32_e32 v164, v164
	v_rcp_f32_e32 v165, v165
	v_rcp_f32_e32 v166, v166
	v_rcp_f32_e32 v167, v167
	v_cvt_f32_ubyte0_e32 v168, v184
	v_cvt_f32_ubyte1_e32 v169, v184
	v_cvt_f32_ubyte2_e32 v170, v184
	v_cvt_f32_ubyte3_e32 v171, v184
	v_cvt_f32_ubyte0_e32 v172, v185
	v_cvt_f32_ubyte1_e32 v173, v185
	v_cvt_f32_ubyte2_e32 v174, v185
	v_cvt_f32_ubyte3_e32 v175, v185
	v_mul_f32_e32 v168, 0x3b808081, v168
	v_mul_f32_e32 v169, 0x3b808081, v169
	v_mul_f32_e32 v170, 0x3b808081, v170
	v_mul_f32_e32 v171, 0x3b808081, v171
	v_mul_f32_e32 v172, 0x3b808081, v172
	v_mul_f32_e32 v173, 0x3b808081, v173
	v_mul_f32_e32 v174, 0x3b808081, v174
	v_mul_f32_e32 v175, 0x3b808081, v175
	v_mul_f32_e32 v168, v160, v168
	v_mul_f32_e32 v169, v161, v169
	v_mul_f32_e32 v170, v162, v170
	v_mul_f32_e32 v171, v163, v171
	v_mul_f32_e32 v172, v164, v172
	v_mul_f32_e32 v173, v165, v173
	v_mul_f32_e32 v174, v166, v174
	v_mul_f32_e32 v175, v167, v175
	v_mul_f32_e32 v34, v34, v168
	v_mul_f32_e32 v35, v35, v169
	v_mul_f32_e32 v36, v36, v170
	v_mul_f32_e32 v37, v37, v171
	v_mul_f32_e32 v30, v30, v172
	v_mul_f32_e32 v31, v31, v173
	v_mul_f32_e32 v32, v32, v174
	v_mul_f32_e32 v33, v33, v175
	s_waitcnt vmcnt(10)
	v_cvt_f32_ubyte0_e32 v160, v186
	v_cvt_f32_ubyte1_e32 v161, v186
	v_cvt_f32_ubyte2_e32 v162, v186
	v_cvt_f32_ubyte3_e32 v163, v186
	v_cvt_f32_ubyte0_e32 v164, v187
	v_cvt_f32_ubyte1_e32 v165, v187
	v_cvt_f32_ubyte2_e32 v166, v187
	v_cvt_f32_ubyte3_e32 v167, v187
	v_mul_f32_e32 v160, 0x3b808081, v160
	v_mul_f32_e32 v161, 0x3b808081, v161
	v_mul_f32_e32 v162, 0x3b808081, v162
	v_mul_f32_e32 v163, 0x3b808081, v163
	v_mul_f32_e32 v164, 0x3b808081, v164
	v_mul_f32_e32 v165, 0x3b808081, v165
	v_mul_f32_e32 v166, 0x3b808081, v166
	v_mul_f32_e32 v167, 0x3b808081, v167
	v_max_f32_e32 v160, 0xda24260, v160
	v_max_f32_e32 v161, 0xda24260, v161
	v_max_f32_e32 v162, 0xda24260, v162
	v_max_f32_e32 v163, 0xda24260, v163
	v_max_f32_e32 v164, 0xda24260, v164
	v_max_f32_e32 v165, 0xda24260, v165
	v_max_f32_e32 v166, 0xda24260, v166
	v_max_f32_e32 v167, 0xda24260, v167
	v_rcp_f32_e32 v160, v160
	v_rcp_f32_e32 v161, v161
	v_rcp_f32_e32 v162, v162
	v_rcp_f32_e32 v163, v163
	v_rcp_f32_e32 v164, v164
	v_rcp_f32_e32 v165, v165
	v_rcp_f32_e32 v166, v166
	v_rcp_f32_e32 v167, v167
	v_cvt_f32_ubyte0_e32 v168, v188
	v_cvt_f32_ubyte1_e32 v169, v188
	v_cvt_f32_ubyte2_e32 v170, v188
	v_cvt_f32_ubyte3_e32 v171, v188
	v_cvt_f32_ubyte0_e32 v172, v189
	v_cvt_f32_ubyte1_e32 v173, v189
	v_cvt_f32_ubyte2_e32 v174, v189
	v_cvt_f32_ubyte3_e32 v175, v189
	v_mul_f32_e32 v168, 0x3b808081, v168
	v_mul_f32_e32 v169, 0x3b808081, v169
	v_mul_f32_e32 v170, 0x3b808081, v170
	v_mul_f32_e32 v171, 0x3b808081, v171
	v_mul_f32_e32 v172, 0x3b808081, v172
	v_mul_f32_e32 v173, 0x3b808081, v173
	v_mul_f32_e32 v174, 0x3b808081, v174
	v_mul_f32_e32 v175, 0x3b808081, v175
	v_mul_f32_e32 v168, v160, v168
	v_mul_f32_e32 v169, v161, v169
	v_mul_f32_e32 v170, v162, v170
	v_mul_f32_e32 v171, v163, v171
	v_mul_f32_e32 v172, v164, v172
	v_mul_f32_e32 v173, v165, v173
	v_mul_f32_e32 v174, v166, v174
	v_mul_f32_e32 v175, v167, v175
	v_mul_f32_e32 v58, v58, v168
	v_mul_f32_e32 v59, v59, v169
	v_mul_f32_e32 v60, v60, v170
	v_mul_f32_e32 v61, v61, v171
	v_mul_f32_e32 v54, v54, v172
	v_mul_f32_e32 v55, v55, v173
	v_mul_f32_e32 v56, v56, v174
	v_mul_f32_e32 v57, v57, v175
	s_waitcnt vmcnt(8)
	v_cvt_f32_ubyte0_e32 v160, v190
	v_cvt_f32_ubyte1_e32 v161, v190
	v_cvt_f32_ubyte2_e32 v162, v190
	v_cvt_f32_ubyte3_e32 v163, v190
	v_cvt_f32_ubyte0_e32 v164, v191
	v_cvt_f32_ubyte1_e32 v165, v191
	v_cvt_f32_ubyte2_e32 v166, v191
	v_cvt_f32_ubyte3_e32 v167, v191
	v_mul_f32_e32 v160, 0x3b808081, v160
	v_mul_f32_e32 v161, 0x3b808081, v161
	v_mul_f32_e32 v162, 0x3b808081, v162
	v_mul_f32_e32 v163, 0x3b808081, v163
	v_mul_f32_e32 v164, 0x3b808081, v164
	v_mul_f32_e32 v165, 0x3b808081, v165
	v_mul_f32_e32 v166, 0x3b808081, v166
	v_mul_f32_e32 v167, 0x3b808081, v167
	v_max_f32_e32 v160, 0xda24260, v160
	v_max_f32_e32 v161, 0xda24260, v161
	v_max_f32_e32 v162, 0xda24260, v162
	v_max_f32_e32 v163, 0xda24260, v163
	v_max_f32_e32 v164, 0xda24260, v164
	v_max_f32_e32 v165, 0xda24260, v165
	v_max_f32_e32 v166, 0xda24260, v166
	v_max_f32_e32 v167, 0xda24260, v167
	v_rcp_f32_e32 v160, v160
	v_rcp_f32_e32 v161, v161
	v_rcp_f32_e32 v162, v162
	v_rcp_f32_e32 v163, v163
	v_rcp_f32_e32 v164, v164
	v_rcp_f32_e32 v165, v165
	v_rcp_f32_e32 v166, v166
	v_rcp_f32_e32 v167, v167
	v_cvt_f32_ubyte0_e32 v168, v192
	v_cvt_f32_ubyte1_e32 v169, v192
	v_cvt_f32_ubyte2_e32 v170, v192
	v_cvt_f32_ubyte3_e32 v171, v192
	v_cvt_f32_ubyte0_e32 v172, v193
	v_cvt_f32_ubyte1_e32 v173, v193
	v_cvt_f32_ubyte2_e32 v174, v193
	v_cvt_f32_ubyte3_e32 v175, v193
	v_mul_f32_e32 v168, 0x3b808081, v168
	v_mul_f32_e32 v169, 0x3b808081, v169
	v_mul_f32_e32 v170, 0x3b808081, v170
	v_mul_f32_e32 v171, 0x3b808081, v171
	v_mul_f32_e32 v172, 0x3b808081, v172
	v_mul_f32_e32 v173, 0x3b808081, v173
	v_mul_f32_e32 v174, 0x3b808081, v174
	v_mul_f32_e32 v175, 0x3b808081, v175
	v_mul_f32_e32 v168, v160, v168
	v_mul_f32_e32 v169, v161, v169
	v_mul_f32_e32 v170, v162, v170
	v_mul_f32_e32 v171, v163, v171
	v_mul_f32_e32 v172, v164, v172
	v_mul_f32_e32 v173, v165, v173
	v_mul_f32_e32 v174, v166, v174
	v_mul_f32_e32 v175, v167, v175
	v_mul_f32_e32 v26, v26, v168
	v_mul_f32_e32 v27, v27, v169
	v_mul_f32_e32 v28, v28, v170
	v_mul_f32_e32 v29, v29, v171
	v_mul_f32_e32 v22, v22, v172
	v_mul_f32_e32 v23, v23, v173
	v_mul_f32_e32 v24, v24, v174
	v_mul_f32_e32 v25, v25, v175
	s_waitcnt vmcnt(6)
	v_cvt_f32_ubyte0_e32 v160, v194
	v_cvt_f32_ubyte1_e32 v161, v194
	v_cvt_f32_ubyte2_e32 v162, v194
	v_cvt_f32_ubyte3_e32 v163, v194
	v_cvt_f32_ubyte0_e32 v164, v195
	v_cvt_f32_ubyte1_e32 v165, v195
	v_cvt_f32_ubyte2_e32 v166, v195
	v_cvt_f32_ubyte3_e32 v167, v195
	v_mul_f32_e32 v160, 0x3b808081, v160
	v_mul_f32_e32 v161, 0x3b808081, v161
	v_mul_f32_e32 v162, 0x3b808081, v162
	v_mul_f32_e32 v163, 0x3b808081, v163
	v_mul_f32_e32 v164, 0x3b808081, v164
	v_mul_f32_e32 v165, 0x3b808081, v165
	v_mul_f32_e32 v166, 0x3b808081, v166
	v_mul_f32_e32 v167, 0x3b808081, v167
	v_max_f32_e32 v160, 0xda24260, v160
	v_max_f32_e32 v161, 0xda24260, v161
	v_max_f32_e32 v162, 0xda24260, v162
	v_max_f32_e32 v163, 0xda24260, v163
	v_max_f32_e32 v164, 0xda24260, v164
	v_max_f32_e32 v165, 0xda24260, v165
	v_max_f32_e32 v166, 0xda24260, v166
	v_max_f32_e32 v167, 0xda24260, v167
	v_rcp_f32_e32 v160, v160
	v_rcp_f32_e32 v161, v161
	v_rcp_f32_e32 v162, v162
	v_rcp_f32_e32 v163, v163
	v_rcp_f32_e32 v164, v164
	v_rcp_f32_e32 v165, v165
	v_rcp_f32_e32 v166, v166
	v_rcp_f32_e32 v167, v167
	v_cvt_f32_ubyte0_e32 v168, v196
	v_cvt_f32_ubyte1_e32 v169, v196
	v_cvt_f32_ubyte2_e32 v170, v196
	v_cvt_f32_ubyte3_e32 v171, v196
	v_cvt_f32_ubyte0_e32 v172, v197
	v_cvt_f32_ubyte1_e32 v173, v197
	v_cvt_f32_ubyte2_e32 v174, v197
	v_cvt_f32_ubyte3_e32 v175, v197
	v_mul_f32_e32 v168, 0x3b808081, v168
	v_mul_f32_e32 v169, 0x3b808081, v169
	v_mul_f32_e32 v170, 0x3b808081, v170
	v_mul_f32_e32 v171, 0x3b808081, v171
	v_mul_f32_e32 v172, 0x3b808081, v172
	v_mul_f32_e32 v173, 0x3b808081, v173
	v_mul_f32_e32 v174, 0x3b808081, v174
	v_mul_f32_e32 v175, 0x3b808081, v175
	v_mul_f32_e32 v168, v160, v168
	v_mul_f32_e32 v169, v161, v169
	v_mul_f32_e32 v170, v162, v170
	v_mul_f32_e32 v171, v163, v171
	v_mul_f32_e32 v172, v164, v172
	v_mul_f32_e32 v173, v165, v173
	v_mul_f32_e32 v174, v166, v174
	v_mul_f32_e32 v175, v167, v175
	v_mul_f32_e32 v50, v50, v168
	v_mul_f32_e32 v51, v51, v169
	v_mul_f32_e32 v52, v52, v170
	v_mul_f32_e32 v53, v53, v171
	v_mul_f32_e32 v46, v46, v172
	v_mul_f32_e32 v47, v47, v173
	v_mul_f32_e32 v48, v48, v174
	v_mul_f32_e32 v49, v49, v175
	s_waitcnt vmcnt(4)
	v_cvt_f32_ubyte0_e32 v160, v198
	v_cvt_f32_ubyte1_e32 v161, v198
	v_cvt_f32_ubyte2_e32 v162, v198
	v_cvt_f32_ubyte3_e32 v163, v198
	v_cvt_f32_ubyte0_e32 v164, v199
	v_cvt_f32_ubyte1_e32 v165, v199
	v_cvt_f32_ubyte2_e32 v166, v199
	v_cvt_f32_ubyte3_e32 v167, v199
	v_mul_f32_e32 v160, 0x3b808081, v160
	v_mul_f32_e32 v161, 0x3b808081, v161
	v_mul_f32_e32 v162, 0x3b808081, v162
	v_mul_f32_e32 v163, 0x3b808081, v163
	v_mul_f32_e32 v164, 0x3b808081, v164
	v_mul_f32_e32 v165, 0x3b808081, v165
	v_mul_f32_e32 v166, 0x3b808081, v166
	v_mul_f32_e32 v167, 0x3b808081, v167
	v_max_f32_e32 v160, 0xda24260, v160
	v_max_f32_e32 v161, 0xda24260, v161
	v_max_f32_e32 v162, 0xda24260, v162
	v_max_f32_e32 v163, 0xda24260, v163
	v_max_f32_e32 v164, 0xda24260, v164
	v_max_f32_e32 v165, 0xda24260, v165
	v_max_f32_e32 v166, 0xda24260, v166
	v_max_f32_e32 v167, 0xda24260, v167
	v_rcp_f32_e32 v160, v160
	v_rcp_f32_e32 v161, v161
	v_rcp_f32_e32 v162, v162
	v_rcp_f32_e32 v163, v163
	v_rcp_f32_e32 v164, v164
	v_rcp_f32_e32 v165, v165
	v_rcp_f32_e32 v166, v166
	v_rcp_f32_e32 v167, v167
	v_cvt_f32_ubyte0_e32 v168, v202
	v_cvt_f32_ubyte1_e32 v169, v202
	v_cvt_f32_ubyte2_e32 v170, v202
	v_cvt_f32_ubyte3_e32 v171, v202
	v_cvt_f32_ubyte0_e32 v172, v203
	v_cvt_f32_ubyte1_e32 v173, v203
	v_cvt_f32_ubyte2_e32 v174, v203
	v_cvt_f32_ubyte3_e32 v175, v203
	v_mul_f32_e32 v168, 0x3b808081, v168
	v_mul_f32_e32 v169, 0x3b808081, v169
	v_mul_f32_e32 v170, 0x3b808081, v170
	v_mul_f32_e32 v171, 0x3b808081, v171
	v_mul_f32_e32 v172, 0x3b808081, v172
	v_mul_f32_e32 v173, 0x3b808081, v173
	v_mul_f32_e32 v174, 0x3b808081, v174
	v_mul_f32_e32 v175, 0x3b808081, v175
	v_mul_f32_e32 v168, v160, v168
	v_mul_f32_e32 v169, v161, v169
	v_mul_f32_e32 v170, v162, v170
	v_mul_f32_e32 v171, v163, v171
	v_mul_f32_e32 v172, v164, v172
	v_mul_f32_e32 v173, v165, v173
	v_mul_f32_e32 v174, v166, v174
	v_mul_f32_e32 v175, v167, v175
	v_mul_f32_e32 v18, v18, v168
	v_mul_f32_e32 v19, v19, v169
	v_mul_f32_e32 v20, v20, v170
	v_mul_f32_e32 v21, v21, v171
	v_mul_f32_e32 v14, v14, v172
	v_mul_f32_e32 v15, v15, v173
	v_mul_f32_e32 v16, v16, v174
	v_mul_f32_e32 v17, v17, v175
	s_waitcnt vmcnt(2)
	v_cvt_f32_ubyte0_e32 v160, v204
	v_cvt_f32_ubyte1_e32 v161, v204
	v_cvt_f32_ubyte2_e32 v162, v204
	v_cvt_f32_ubyte3_e32 v163, v204
	v_cvt_f32_ubyte0_e32 v164, v205
	v_cvt_f32_ubyte1_e32 v165, v205
	v_cvt_f32_ubyte2_e32 v166, v205
	v_cvt_f32_ubyte3_e32 v167, v205
	v_mul_f32_e32 v160, 0x3b808081, v160
	v_mul_f32_e32 v161, 0x3b808081, v161
	v_mul_f32_e32 v162, 0x3b808081, v162
	v_mul_f32_e32 v163, 0x3b808081, v163
	v_mul_f32_e32 v164, 0x3b808081, v164
	v_mul_f32_e32 v165, 0x3b808081, v165
	v_mul_f32_e32 v166, 0x3b808081, v166
	v_mul_f32_e32 v167, 0x3b808081, v167
	v_max_f32_e32 v160, 0xda24260, v160
	v_max_f32_e32 v161, 0xda24260, v161
	v_max_f32_e32 v162, 0xda24260, v162
	v_max_f32_e32 v163, 0xda24260, v163
	v_max_f32_e32 v164, 0xda24260, v164
	v_max_f32_e32 v165, 0xda24260, v165
	v_max_f32_e32 v166, 0xda24260, v166
	v_max_f32_e32 v167, 0xda24260, v167
	v_rcp_f32_e32 v160, v160
	v_rcp_f32_e32 v161, v161
	v_rcp_f32_e32 v162, v162
	v_rcp_f32_e32 v163, v163
	v_rcp_f32_e32 v164, v164
	v_rcp_f32_e32 v165, v165
	v_rcp_f32_e32 v166, v166
	v_rcp_f32_e32 v167, v167
	v_cvt_f32_ubyte0_e32 v168, v206
	v_cvt_f32_ubyte1_e32 v169, v206
	v_cvt_f32_ubyte2_e32 v170, v206
	v_cvt_f32_ubyte3_e32 v171, v206
	v_cvt_f32_ubyte0_e32 v172, v207
	v_cvt_f32_ubyte1_e32 v173, v207
	v_cvt_f32_ubyte2_e32 v174, v207
	v_cvt_f32_ubyte3_e32 v175, v207
	v_mul_f32_e32 v168, 0x3b808081, v168
	v_mul_f32_e32 v169, 0x3b808081, v169
	v_mul_f32_e32 v170, 0x3b808081, v170
	v_mul_f32_e32 v171, 0x3b808081, v171
	v_mul_f32_e32 v172, 0x3b808081, v172
	v_mul_f32_e32 v173, 0x3b808081, v173
	v_mul_f32_e32 v174, 0x3b808081, v174
	v_mul_f32_e32 v175, 0x3b808081, v175
	v_mul_f32_e32 v168, v160, v168
	v_mul_f32_e32 v169, v161, v169
	v_mul_f32_e32 v170, v162, v170
	v_mul_f32_e32 v171, v163, v171
	v_mul_f32_e32 v172, v164, v172
	v_mul_f32_e32 v173, v165, v173
	v_mul_f32_e32 v174, v166, v174
	v_mul_f32_e32 v175, v167, v175
	v_mul_f32_e32 v42, v42, v168
	v_mul_f32_e32 v43, v43, v169
	v_mul_f32_e32 v44, v44, v170
	v_mul_f32_e32 v45, v45, v171
	v_mul_f32_e32 v38, v38, v172
	v_mul_f32_e32 v39, v39, v173
	v_mul_f32_e32 v40, v40, v174
	v_mul_f32_e32 v41, v41, v175
	s_waitcnt vmcnt(0)
	v_cvt_f32_ubyte0_e32 v160, v208
	v_cvt_f32_ubyte1_e32 v161, v208
	v_cvt_f32_ubyte2_e32 v162, v208
	v_cvt_f32_ubyte3_e32 v163, v208
	v_cvt_f32_ubyte0_e32 v164, v209
	v_cvt_f32_ubyte1_e32 v165, v209
	v_cvt_f32_ubyte2_e32 v166, v209
	v_cvt_f32_ubyte3_e32 v167, v209
	v_mul_f32_e32 v160, 0x3b808081, v160
	v_mul_f32_e32 v161, 0x3b808081, v161
	v_mul_f32_e32 v162, 0x3b808081, v162
	v_mul_f32_e32 v163, 0x3b808081, v163
	v_mul_f32_e32 v164, 0x3b808081, v164
	v_mul_f32_e32 v165, 0x3b808081, v165
	v_mul_f32_e32 v166, 0x3b808081, v166
	v_mul_f32_e32 v167, 0x3b808081, v167
	v_max_f32_e32 v160, 0xda24260, v160
	v_max_f32_e32 v161, 0xda24260, v161
	v_max_f32_e32 v162, 0xda24260, v162
	v_max_f32_e32 v163, 0xda24260, v163
	v_max_f32_e32 v164, 0xda24260, v164
	v_max_f32_e32 v165, 0xda24260, v165
	v_max_f32_e32 v166, 0xda24260, v166
	v_max_f32_e32 v167, 0xda24260, v167
	v_rcp_f32_e32 v160, v160
	v_rcp_f32_e32 v161, v161
	v_rcp_f32_e32 v162, v162
	v_rcp_f32_e32 v163, v163
	v_rcp_f32_e32 v164, v164
	v_rcp_f32_e32 v165, v165
	v_rcp_f32_e32 v166, v166
	v_rcp_f32_e32 v167, v167
	v_cvt_f32_ubyte0_e32 v168, v210
	v_cvt_f32_ubyte1_e32 v169, v210
	v_cvt_f32_ubyte2_e32 v170, v210
	v_cvt_f32_ubyte3_e32 v171, v210
	v_cvt_f32_ubyte0_e32 v172, v211
	v_cvt_f32_ubyte1_e32 v173, v211
	v_cvt_f32_ubyte2_e32 v174, v211
	v_cvt_f32_ubyte3_e32 v175, v211
	v_mul_f32_e32 v168, 0x3b808081, v168
	v_mul_f32_e32 v169, 0x3b808081, v169
	v_mul_f32_e32 v170, 0x3b808081, v170
	v_mul_f32_e32 v171, 0x3b808081, v171
	v_mul_f32_e32 v172, 0x3b808081, v172
	v_mul_f32_e32 v173, 0x3b808081, v173
	v_mul_f32_e32 v174, 0x3b808081, v174
	v_mul_f32_e32 v175, 0x3b808081, v175
	v_mul_f32_e32 v168, v160, v168
	v_mul_f32_e32 v169, v161, v169
	v_mul_f32_e32 v170, v162, v170
	v_mul_f32_e32 v171, v163, v171
	v_mul_f32_e32 v172, v164, v172
	v_mul_f32_e32 v173, v165, v173
	v_mul_f32_e32 v174, v166, v174
	v_mul_f32_e32 v175, v167, v175
	v_mul_f32_e32 v10, v10, v168
	v_mul_f32_e32 v11, v11, v169
	v_mul_f32_e32 v12, v12, v170
	v_mul_f32_e32 v13, v13, v171
	v_mul_f32_e32 v6, v6, v172
	v_mul_f32_e32 v7, v7, v173
	v_mul_f32_e32 v8, v8, v174
	v_mul_f32_e32 v9, v9, v175
	s_mov_b64 s[6:7], -1
	s_branch .Lp6_done
.Lp6_second:
	global_load_dwordx2 v[178:179], v[176:177], off offset:1024
	global_load_dwordx2 v[180:181], v[176:177], off offset:1152
	v_add_co_u32_e32 v176, vcc, 0x8000, v176
	s_nop 1
	v_addc_co_u32_e32 v177, vcc, 0, v177, vcc
	global_load_dwordx2 v[182:183], v[176:177], off offset:1024
	global_load_dwordx2 v[184:185], v[176:177], off offset:1152
	v_add_co_u32_e32 v176, vcc, 0x8000, v176
	s_nop 1
	v_addc_co_u32_e32 v177, vcc, 0, v177, vcc
	global_load_dwordx2 v[186:187], v[176:177], off offset:1024
	global_load_dwordx2 v[188:189], v[176:177], off offset:1152
	v_add_co_u32_e32 v176, vcc, 0x8000, v176
	s_nop 1
	v_addc_co_u32_e32 v177, vcc, 0, v177, vcc
	global_load_dwordx2 v[190:191], v[176:177], off offset:1024
	global_load_dwordx2 v[192:193], v[176:177], off offset:1152
	v_add_co_u32_e32 v176, vcc, 0x28000, v176
	s_nop 1
	v_addc_co_u32_e32 v177, vcc, 0, v177, vcc
	global_load_dwordx2 v[194:195], v[176:177], off offset:1024
	global_load_dwordx2 v[196:197], v[176:177], off offset:1152
	v_add_co_u32_e32 v176, vcc, 0x8000, v176
	s_nop 1
	v_addc_co_u32_e32 v177, vcc, 0, v177, vcc
	global_load_dwordx2 v[198:199], v[176:177], off offset:1024
	global_load_dwordx2 v[202:203], v[176:177], off offset:1152
	v_add_co_u32_e32 v176, vcc, 0x8000, v176
	s_nop 1
	v_addc_co_u32_e32 v177, vcc, 0, v177, vcc
	global_load_dwordx2 v[204:205], v[176:177], off offset:1024
	global_load_dwordx2 v[206:207], v[176:177], off offset:1152
	v_add_co_u32_e32 v176, vcc, 0x8000, v176
	s_nop 1
	v_addc_co_u32_e32 v177, vcc, 0, v177, vcc
	global_load_dwordx2 v[208:209], v[176:177], off offset:1024
	global_load_dwordx2 v[210:211], v[176:177], off offset:1152
	s_waitcnt vmcnt(15)
	v_cvt_f32_ubyte0_e32 v160, v178
	v_cvt_f32_ubyte1_e32 v161, v178
	v_cvt_f32_ubyte2_e32 v162, v178
	v_cvt_f32_ubyte3_e32 v163, v178
	v_cvt_f32_ubyte0_e32 v164, v179
	v_cvt_f32_ubyte1_e32 v165, v179
	v_cvt_f32_ubyte2_e32 v166, v179
	v_cvt_f32_ubyte3_e32 v167, v179
	v_mul_f32_e32 v160, 0x3b808081, v160
	v_mul_f32_e32 v161, 0x3b808081, v161
	v_mul_f32_e32 v162, 0x3b808081, v162
	v_mul_f32_e32 v163, 0x3b808081, v163
	v_mul_f32_e32 v164, 0x3b808081, v164
	v_mul_f32_e32 v165, 0x3b808081, v165
	v_mul_f32_e32 v166, 0x3b808081, v166
	v_mul_f32_e32 v167, 0x3b808081, v167
	v_max_f32_e32 v160, 0xda24260, v160
	v_max_f32_e32 v161, 0xda24260, v161
	v_max_f32_e32 v162, 0xda24260, v162
	v_max_f32_e32 v163, 0xda24260, v163
	v_max_f32_e32 v164, 0xda24260, v164
	v_max_f32_e32 v165, 0xda24260, v165
	v_max_f32_e32 v166, 0xda24260, v166
	v_max_f32_e32 v167, 0xda24260, v167
	v_mul_f32_e32 v160, v130, v160
	v_mul_f32_e32 v161, v131, v161
	v_mul_f32_e32 v162, v132, v162
	v_mul_f32_e32 v163, v133, v163
	v_mul_f32_e32 v164, v126, v164
	v_mul_f32_e32 v165, v127, v165
	v_mul_f32_e32 v166, v128, v166
	v_mul_f32_e32 v167, v129, v167
	v_cvt_pk_bf16_f32 v168, v160, v161
	v_cvt_pk_bf16_f32 v169, v162, v163
	v_cvt_pk_bf16_f32 v170, v164, v165
	v_cvt_pk_bf16_f32 v171, v166, v167
	global_store_dwordx4 v[174:175], v[168:171], off
	s_waitcnt vmcnt(15)
	v_cvt_f32_ubyte0_e32 v160, v180
	v_cvt_f32_ubyte1_e32 v161, v180
	v_cvt_f32_ubyte2_e32 v162, v180
	v_cvt_f32_ubyte3_e32 v163, v180
	v_cvt_f32_ubyte0_e32 v164, v181
	v_cvt_f32_ubyte1_e32 v165, v181
	v_cvt_f32_ubyte2_e32 v166, v181
	v_cvt_f32_ubyte3_e32 v167, v181
	v_mul_f32_e32 v160, 0x3b808081, v160
	v_mul_f32_e32 v161, 0x3b808081, v161
	v_mul_f32_e32 v162, 0x3b808081, v162
	v_mul_f32_e32 v163, 0x3b808081, v163
	v_mul_f32_e32 v164, 0x3b808081, v164
	v_mul_f32_e32 v165, 0x3b808081, v165
	v_mul_f32_e32 v166, 0x3b808081, v166
	v_mul_f32_e32 v167, 0x3b808081, v167
	v_max_f32_e32 v160, 0xda24260, v160
	v_max_f32_e32 v161, 0xda24260, v161
	v_max_f32_e32 v162, 0xda24260, v162
	v_max_f32_e32 v163, 0xda24260, v163
	v_max_f32_e32 v164, 0xda24260, v164
	v_max_f32_e32 v165, 0xda24260, v165
	v_max_f32_e32 v166, 0xda24260, v166
	v_max_f32_e32 v167, 0xda24260, v167
	v_mul_f32_e32 v160, v98, v160
	v_mul_f32_e32 v161, v99, v161
	v_mul_f32_e32 v162, v100, v162
	v_mul_f32_e32 v163, v101, v163
	v_mul_f32_e32 v164, v94, v164
	v_mul_f32_e32 v165, v95, v165
	v_mul_f32_e32 v166, v96, v166
	v_mul_f32_e32 v167, v97, v167
	v_cvt_pk_bf16_f32 v168, v160, v161
	v_cvt_pk_bf16_f32 v169, v162, v163
	v_cvt_pk_bf16_f32 v170, v164, v165
	v_cvt_pk_bf16_f32 v171, v166, v167
	global_store_dwordx4 v[174:175], v[168:171], off offset:256
	s_waitcnt vmcnt(15)
	v_cvt_f32_ubyte0_e32 v160, v182
	v_cvt_f32_ubyte1_e32 v161, v182
	v_cvt_f32_ubyte2_e32 v162, v182
	v_cvt_f32_ubyte3_e32 v163, v182
	v_cvt_f32_ubyte0_e32 v164, v183
	v_cvt_f32_ubyte1_e32 v165, v183
	v_cvt_f32_ubyte2_e32 v166, v183
	v_cvt_f32_ubyte3_e32 v167, v183
	v_mul_f32_e32 v160, 0x3b808081, v160
	v_mul_f32_e32 v161, 0x3b808081, v161
	v_mul_f32_e32 v162, 0x3b808081, v162
	v_mul_f32_e32 v163, 0x3b808081, v163
	v_mul_f32_e32 v164, 0x3b808081, v164
	v_mul_f32_e32 v165, 0x3b808081, v165
	v_mul_f32_e32 v166, 0x3b808081, v166
	v_mul_f32_e32 v167, 0x3b808081, v167
	v_max_f32_e32 v160, 0xda24260, v160
	v_max_f32_e32 v161, 0xda24260, v161
	v_max_f32_e32 v162, 0xda24260, v162
	v_max_f32_e32 v163, 0xda24260, v163
	v_max_f32_e32 v164, 0xda24260, v164
	v_max_f32_e32 v165, 0xda24260, v165
	v_max_f32_e32 v166, 0xda24260, v166
	v_max_f32_e32 v167, 0xda24260, v167
	v_mul_f32_e32 v160, v122, v160
	v_mul_f32_e32 v161, v123, v161
	v_mul_f32_e32 v162, v124, v162
	v_mul_f32_e32 v163, v125, v163
	v_mul_f32_e32 v164, v118, v164
	v_mul_f32_e32 v165, v119, v165
	v_mul_f32_e32 v166, v120, v166
	v_mul_f32_e32 v167, v121, v167
	v_cvt_pk_bf16_f32 v168, v160, v161
	v_cvt_pk_bf16_f32 v169, v162, v163
	v_cvt_pk_bf16_f32 v170, v164, v165
	v_cvt_pk_bf16_f32 v171, v166, v167
	v_add_co_u32_e32 v174, vcc, 0x8000, v174
	s_nop 1
	v_addc_co_u32_e32 v175, vcc, 0, v175, vcc
	global_store_dwordx4 v[174:175], v[168:171], off
	s_waitcnt vmcnt(15)
	v_cvt_f32_ubyte0_e32 v160, v184
	v_cvt_f32_ubyte1_e32 v161, v184
	v_cvt_f32_ubyte2_e32 v162, v184
	v_cvt_f32_ubyte3_e32 v163, v184
	v_cvt_f32_ubyte0_e32 v164, v185
	v_cvt_f32_ubyte1_e32 v165, v185
	v_cvt_f32_ubyte2_e32 v166, v185
	v_cvt_f32_ubyte3_e32 v167, v185
	v_mul_f32_e32 v160, 0x3b808081, v160
	v_mul_f32_e32 v161, 0x3b808081, v161
	v_mul_f32_e32 v162, 0x3b808081, v162
	v_mul_f32_e32 v163, 0x3b808081, v163
	v_mul_f32_e32 v164, 0x3b808081, v164
	v_mul_f32_e32 v165, 0x3b808081, v165
	v_mul_f32_e32 v166, 0x3b808081, v166
	v_mul_f32_e32 v167, 0x3b808081, v167
	v_max_f32_e32 v160, 0xda24260, v160
	v_max_f32_e32 v161, 0xda24260, v161
	v_max_f32_e32 v162, 0xda24260, v162
	v_max_f32_e32 v163, 0xda24260, v163
	v_max_f32_e32 v164, 0xda24260, v164
	v_max_f32_e32 v165, 0xda24260, v165
	v_max_f32_e32 v166, 0xda24260, v166
	v_max_f32_e32 v167, 0xda24260, v167
	v_mul_f32_e32 v160, v90, v160
	v_mul_f32_e32 v161, v91, v161
	v_mul_f32_e32 v162, v92, v162
	v_mul_f32_e32 v163, v93, v163
	v_mul_f32_e32 v164, v86, v164
	v_mul_f32_e32 v165, v87, v165
	v_mul_f32_e32 v166, v88, v166
	v_mul_f32_e32 v167, v89, v167
	v_cvt_pk_bf16_f32 v168, v160, v161
	v_cvt_pk_bf16_f32 v169, v162, v163
	v_cvt_pk_bf16_f32 v170, v164, v165
	v_cvt_pk_bf16_f32 v171, v166, v167
	global_store_dwordx4 v[174:175], v[168:171], off offset:256
	s_waitcnt vmcnt(15)
	v_cvt_f32_ubyte0_e32 v160, v186
	v_cvt_f32_ubyte1_e32 v161, v186
	v_cvt_f32_ubyte2_e32 v162, v186
	v_cvt_f32_ubyte3_e32 v163, v186
	v_cvt_f32_ubyte0_e32 v164, v187
	v_cvt_f32_ubyte1_e32 v165, v187
	v_cvt_f32_ubyte2_e32 v166, v187
	v_cvt_f32_ubyte3_e32 v167, v187
	v_mul_f32_e32 v160, 0x3b808081, v160
	v_mul_f32_e32 v161, 0x3b808081, v161
	v_mul_f32_e32 v162, 0x3b808081, v162
	v_mul_f32_e32 v163, 0x3b808081, v163
	v_mul_f32_e32 v164, 0x3b808081, v164
	v_mul_f32_e32 v165, 0x3b808081, v165
	v_mul_f32_e32 v166, 0x3b808081, v166
	v_mul_f32_e32 v167, 0x3b808081, v167
	v_max_f32_e32 v160, 0xda24260, v160
	v_max_f32_e32 v161, 0xda24260, v161
	v_max_f32_e32 v162, 0xda24260, v162
	v_max_f32_e32 v163, 0xda24260, v163
	v_max_f32_e32 v164, 0xda24260, v164
	v_max_f32_e32 v165, 0xda24260, v165
	v_max_f32_e32 v166, 0xda24260, v166
	v_max_f32_e32 v167, 0xda24260, v167
	v_mul_f32_e32 v160, v114, v160
	v_mul_f32_e32 v161, v115, v161
	v_mul_f32_e32 v162, v116, v162
	v_mul_f32_e32 v163, v117, v163
	v_mul_f32_e32 v164, v110, v164
	v_mul_f32_e32 v165, v111, v165
	v_mul_f32_e32 v166, v112, v166
	v_mul_f32_e32 v167, v113, v167
	v_cvt_pk_bf16_f32 v168, v160, v161
	v_cvt_pk_bf16_f32 v169, v162, v163
	v_cvt_pk_bf16_f32 v170, v164, v165
	v_cvt_pk_bf16_f32 v171, v166, v167
	v_add_co_u32_e32 v174, vcc, 0x8000, v174
	s_nop 1
	v_addc_co_u32_e32 v175, vcc, 0, v175, vcc
	global_store_dwordx4 v[174:175], v[168:171], off
	s_waitcnt vmcnt(15)
	v_cvt_f32_ubyte0_e32 v160, v188
	v_cvt_f32_ubyte1_e32 v161, v188
	v_cvt_f32_ubyte2_e32 v162, v188
	v_cvt_f32_ubyte3_e32 v163, v188
	v_cvt_f32_ubyte0_e32 v164, v189
	v_cvt_f32_ubyte1_e32 v165, v189
	v_cvt_f32_ubyte2_e32 v166, v189
	v_cvt_f32_ubyte3_e32 v167, v189
	v_mul_f32_e32 v160, 0x3b808081, v160
	v_mul_f32_e32 v161, 0x3b808081, v161
	v_mul_f32_e32 v162, 0x3b808081, v162
	v_mul_f32_e32 v163, 0x3b808081, v163
	v_mul_f32_e32 v164, 0x3b808081, v164
	v_mul_f32_e32 v165, 0x3b808081, v165
	v_mul_f32_e32 v166, 0x3b808081, v166
	v_mul_f32_e32 v167, 0x3b808081, v167
	v_max_f32_e32 v160, 0xda24260, v160
	v_max_f32_e32 v161, 0xda24260, v161
	v_max_f32_e32 v162, 0xda24260, v162
	v_max_f32_e32 v163, 0xda24260, v163
	v_max_f32_e32 v164, 0xda24260, v164
	v_max_f32_e32 v165, 0xda24260, v165
	v_max_f32_e32 v166, 0xda24260, v166
	v_max_f32_e32 v167, 0xda24260, v167
	v_mul_f32_e32 v160, v82, v160
	v_mul_f32_e32 v161, v83, v161
	v_mul_f32_e32 v162, v84, v162
	v_mul_f32_e32 v163, v85, v163
	v_mul_f32_e32 v164, v78, v164
	v_mul_f32_e32 v165, v79, v165
	v_mul_f32_e32 v166, v80, v166
	v_mul_f32_e32 v167, v81, v167
	v_cvt_pk_bf16_f32 v168, v160, v161
	v_cvt_pk_bf16_f32 v169, v162, v163
	v_cvt_pk_bf16_f32 v170, v164, v165
	v_cvt_pk_bf16_f32 v171, v166, v167
	global_store_dwordx4 v[174:175], v[168:171], off offset:256
	s_waitcnt vmcnt(15)
	v_cvt_f32_ubyte0_e32 v160, v190
	v_cvt_f32_ubyte1_e32 v161, v190
	v_cvt_f32_ubyte2_e32 v162, v190
	v_cvt_f32_ubyte3_e32 v163, v190
	v_cvt_f32_ubyte0_e32 v164, v191
	v_cvt_f32_ubyte1_e32 v165, v191
	v_cvt_f32_ubyte2_e32 v166, v191
	v_cvt_f32_ubyte3_e32 v167, v191
	v_mul_f32_e32 v160, 0x3b808081, v160
	v_mul_f32_e32 v161, 0x3b808081, v161
	v_mul_f32_e32 v162, 0x3b808081, v162
	v_mul_f32_e32 v163, 0x3b808081, v163
	v_mul_f32_e32 v164, 0x3b808081, v164
	v_mul_f32_e32 v165, 0x3b808081, v165
	v_mul_f32_e32 v166, 0x3b808081, v166
	v_mul_f32_e32 v167, 0x3b808081, v167
	v_max_f32_e32 v160, 0xda24260, v160
	v_max_f32_e32 v161, 0xda24260, v161
	v_max_f32_e32 v162, 0xda24260, v162
	v_max_f32_e32 v163, 0xda24260, v163
	v_max_f32_e32 v164, 0xda24260, v164
	v_max_f32_e32 v165, 0xda24260, v165
	v_max_f32_e32 v166, 0xda24260, v166
	v_max_f32_e32 v167, 0xda24260, v167
	v_mul_f32_e32 v160, v106, v160
	v_mul_f32_e32 v161, v107, v161
	v_mul_f32_e32 v162, v108, v162
	v_mul_f32_e32 v163, v109, v163
	v_mul_f32_e32 v164, v102, v164
	v_mul_f32_e32 v165, v103, v165
	v_mul_f32_e32 v166, v104, v166
	v_mul_f32_e32 v167, v105, v167
	v_cvt_pk_bf16_f32 v168, v160, v161
	v_cvt_pk_bf16_f32 v169, v162, v163
	v_cvt_pk_bf16_f32 v170, v164, v165
	v_cvt_pk_bf16_f32 v171, v166, v167
	v_add_co_u32_e32 v174, vcc, 0x8000, v174
	s_nop 1
	v_addc_co_u32_e32 v175, vcc, 0, v175, vcc
	global_store_dwordx4 v[174:175], v[168:171], off
	s_waitcnt vmcnt(15)
	v_cvt_f32_ubyte0_e32 v160, v192
	v_cvt_f32_ubyte1_e32 v161, v192
	v_cvt_f32_ubyte2_e32 v162, v192
	v_cvt_f32_ubyte3_e32 v163, v192
	v_cvt_f32_ubyte0_e32 v164, v193
	v_cvt_f32_ubyte1_e32 v165, v193
	v_cvt_f32_ubyte2_e32 v166, v193
	v_cvt_f32_ubyte3_e32 v167, v193
	v_mul_f32_e32 v160, 0x3b808081, v160
	v_mul_f32_e32 v161, 0x3b808081, v161
	v_mul_f32_e32 v162, 0x3b808081, v162
	v_mul_f32_e32 v163, 0x3b808081, v163
	v_mul_f32_e32 v164, 0x3b808081, v164
	v_mul_f32_e32 v165, 0x3b808081, v165
	v_mul_f32_e32 v166, 0x3b808081, v166
	v_mul_f32_e32 v167, 0x3b808081, v167
	v_max_f32_e32 v160, 0xda24260, v160
	v_max_f32_e32 v161, 0xda24260, v161
	v_max_f32_e32 v162, 0xda24260, v162
	v_max_f32_e32 v163, 0xda24260, v163
	v_max_f32_e32 v164, 0xda24260, v164
	v_max_f32_e32 v165, 0xda24260, v165
	v_max_f32_e32 v166, 0xda24260, v166
	v_max_f32_e32 v167, 0xda24260, v167
	v_mul_f32_e32 v160, v74, v160
	v_mul_f32_e32 v161, v75, v161
	v_mul_f32_e32 v162, v76, v162
	v_mul_f32_e32 v163, v77, v163
	v_mul_f32_e32 v164, v70, v164
	v_mul_f32_e32 v165, v71, v165
	v_mul_f32_e32 v166, v72, v166
	v_mul_f32_e32 v167, v73, v167
	v_cvt_pk_bf16_f32 v168, v160, v161
	v_cvt_pk_bf16_f32 v169, v162, v163
	v_cvt_pk_bf16_f32 v170, v164, v165
	v_cvt_pk_bf16_f32 v171, v166, v167
	global_store_dwordx4 v[174:175], v[168:171], off offset:256
	s_waitcnt vmcnt(15)
	v_cvt_f32_ubyte0_e32 v160, v194
	v_cvt_f32_ubyte1_e32 v161, v194
	v_cvt_f32_ubyte2_e32 v162, v194
	v_cvt_f32_ubyte3_e32 v163, v194
	v_cvt_f32_ubyte0_e32 v164, v195
	v_cvt_f32_ubyte1_e32 v165, v195
	v_cvt_f32_ubyte2_e32 v166, v195
	v_cvt_f32_ubyte3_e32 v167, v195
	v_mul_f32_e32 v160, 0x3b808081, v160
	v_mul_f32_e32 v161, 0x3b808081, v161
	v_mul_f32_e32 v162, 0x3b808081, v162
	v_mul_f32_e32 v163, 0x3b808081, v163
	v_mul_f32_e32 v164, 0x3b808081, v164
	v_mul_f32_e32 v165, 0x3b808081, v165
	v_mul_f32_e32 v166, 0x3b808081, v166
	v_mul_f32_e32 v167, 0x3b808081, v167
	v_max_f32_e32 v160, 0xda24260, v160
	v_max_f32_e32 v161, 0xda24260, v161
	v_max_f32_e32 v162, 0xda24260, v162
	v_max_f32_e32 v163, 0xda24260, v163
	v_max_f32_e32 v164, 0xda24260, v164
	v_max_f32_e32 v165, 0xda24260, v165
	v_max_f32_e32 v166, 0xda24260, v166
	v_max_f32_e32 v167, 0xda24260, v167
	v_mul_f32_e32 v160, v66, v160
	v_mul_f32_e32 v161, v67, v161
	v_mul_f32_e32 v162, v68, v162
	v_mul_f32_e32 v163, v69, v163
	v_mul_f32_e32 v164, v62, v164
	v_mul_f32_e32 v165, v63, v165
	v_mul_f32_e32 v166, v64, v166
	v_mul_f32_e32 v167, v65, v167
	v_cvt_pk_bf16_f32 v168, v160, v161
	v_cvt_pk_bf16_f32 v169, v162, v163
	v_cvt_pk_bf16_f32 v170, v164, v165
	v_cvt_pk_bf16_f32 v171, v166, v167
	v_add_co_u32_e32 v174, vcc, 0x28000, v174
	s_nop 1
	v_addc_co_u32_e32 v175, vcc, 0, v175, vcc
	global_store_dwordx4 v[174:175], v[168:171], off
	s_waitcnt vmcnt(15)
	v_cvt_f32_ubyte0_e32 v160, v196
	v_cvt_f32_ubyte1_e32 v161, v196
	v_cvt_f32_ubyte2_e32 v162, v196
	v_cvt_f32_ubyte3_e32 v163, v196
	v_cvt_f32_ubyte0_e32 v164, v197
	v_cvt_f32_ubyte1_e32 v165, v197
	v_cvt_f32_ubyte2_e32 v166, v197
	v_cvt_f32_ubyte3_e32 v167, v197
	v_mul_f32_e32 v160, 0x3b808081, v160
	v_mul_f32_e32 v161, 0x3b808081, v161
	v_mul_f32_e32 v162, 0x3b808081, v162
	v_mul_f32_e32 v163, 0x3b808081, v163
	v_mul_f32_e32 v164, 0x3b808081, v164
	v_mul_f32_e32 v165, 0x3b808081, v165
	v_mul_f32_e32 v166, 0x3b808081, v166
	v_mul_f32_e32 v167, 0x3b808081, v167
	v_max_f32_e32 v160, 0xda24260, v160
	v_max_f32_e32 v161, 0xda24260, v161
	v_max_f32_e32 v162, 0xda24260, v162
	v_max_f32_e32 v163, 0xda24260, v163
	v_max_f32_e32 v164, 0xda24260, v164
	v_max_f32_e32 v165, 0xda24260, v165
	v_max_f32_e32 v166, 0xda24260, v166
	v_max_f32_e32 v167, 0xda24260, v167
	v_mul_f32_e32 v160, v34, v160
	v_mul_f32_e32 v161, v35, v161
	v_mul_f32_e32 v162, v36, v162
	v_mul_f32_e32 v163, v37, v163
	v_mul_f32_e32 v164, v30, v164
	v_mul_f32_e32 v165, v31, v165
	v_mul_f32_e32 v166, v32, v166
	v_mul_f32_e32 v167, v33, v167
	v_cvt_pk_bf16_f32 v168, v160, v161
	v_cvt_pk_bf16_f32 v169, v162, v163
	v_cvt_pk_bf16_f32 v170, v164, v165
	v_cvt_pk_bf16_f32 v171, v166, v167
	global_store_dwordx4 v[174:175], v[168:171], off offset:256
	s_waitcnt vmcnt(15)
	v_cvt_f32_ubyte0_e32 v160, v198
	v_cvt_f32_ubyte1_e32 v161, v198
	v_cvt_f32_ubyte2_e32 v162, v198
	v_cvt_f32_ubyte3_e32 v163, v198
	v_cvt_f32_ubyte0_e32 v164, v199
	v_cvt_f32_ubyte1_e32 v165, v199
	v_cvt_f32_ubyte2_e32 v166, v199
	v_cvt_f32_ubyte3_e32 v167, v199
	v_mul_f32_e32 v160, 0x3b808081, v160
	v_mul_f32_e32 v161, 0x3b808081, v161
	v_mul_f32_e32 v162, 0x3b808081, v162
	v_mul_f32_e32 v163, 0x3b808081, v163
	v_mul_f32_e32 v164, 0x3b808081, v164
	v_mul_f32_e32 v165, 0x3b808081, v165
	v_mul_f32_e32 v166, 0x3b808081, v166
	v_mul_f32_e32 v167, 0x3b808081, v167
	v_max_f32_e32 v160, 0xda24260, v160
	v_max_f32_e32 v161, 0xda24260, v161
	v_max_f32_e32 v162, 0xda24260, v162
	v_max_f32_e32 v163, 0xda24260, v163
	v_max_f32_e32 v164, 0xda24260, v164
	v_max_f32_e32 v165, 0xda24260, v165
	v_max_f32_e32 v166, 0xda24260, v166
	v_max_f32_e32 v167, 0xda24260, v167
	v_mul_f32_e32 v160, v58, v160
	v_mul_f32_e32 v161, v59, v161
	v_mul_f32_e32 v162, v60, v162
	v_mul_f32_e32 v163, v61, v163
	v_mul_f32_e32 v164, v54, v164
	v_mul_f32_e32 v165, v55, v165
	v_mul_f32_e32 v166, v56, v166
	v_mul_f32_e32 v167, v57, v167
	v_cvt_pk_bf16_f32 v168, v160, v161
	v_cvt_pk_bf16_f32 v169, v162, v163
	v_cvt_pk_bf16_f32 v170, v164, v165
	v_cvt_pk_bf16_f32 v171, v166, v167
	v_add_co_u32_e32 v174, vcc, 0x8000, v174
	s_nop 1
	v_addc_co_u32_e32 v175, vcc, 0, v175, vcc
	global_store_dwordx4 v[174:175], v[168:171], off
	s_waitcnt vmcnt(15)
	v_cvt_f32_ubyte0_e32 v160, v202
	v_cvt_f32_ubyte1_e32 v161, v202
	v_cvt_f32_ubyte2_e32 v162, v202
	v_cvt_f32_ubyte3_e32 v163, v202
	v_cvt_f32_ubyte0_e32 v164, v203
	v_cvt_f32_ubyte1_e32 v165, v203
	v_cvt_f32_ubyte2_e32 v166, v203
	v_cvt_f32_ubyte3_e32 v167, v203
	v_mul_f32_e32 v160, 0x3b808081, v160
	v_mul_f32_e32 v161, 0x3b808081, v161
	v_mul_f32_e32 v162, 0x3b808081, v162
	v_mul_f32_e32 v163, 0x3b808081, v163
	v_mul_f32_e32 v164, 0x3b808081, v164
	v_mul_f32_e32 v165, 0x3b808081, v165
	v_mul_f32_e32 v166, 0x3b808081, v166
	v_mul_f32_e32 v167, 0x3b808081, v167
	v_max_f32_e32 v160, 0xda24260, v160
	v_max_f32_e32 v161, 0xda24260, v161
	v_max_f32_e32 v162, 0xda24260, v162
	v_max_f32_e32 v163, 0xda24260, v163
	v_max_f32_e32 v164, 0xda24260, v164
	v_max_f32_e32 v165, 0xda24260, v165
	v_max_f32_e32 v166, 0xda24260, v166
	v_max_f32_e32 v167, 0xda24260, v167
	v_mul_f32_e32 v160, v26, v160
	v_mul_f32_e32 v161, v27, v161
	v_mul_f32_e32 v162, v28, v162
	v_mul_f32_e32 v163, v29, v163
	v_mul_f32_e32 v164, v22, v164
	v_mul_f32_e32 v165, v23, v165
	v_mul_f32_e32 v166, v24, v166
	v_mul_f32_e32 v167, v25, v167
	v_cvt_pk_bf16_f32 v168, v160, v161
	v_cvt_pk_bf16_f32 v169, v162, v163
	v_cvt_pk_bf16_f32 v170, v164, v165
	v_cvt_pk_bf16_f32 v171, v166, v167
	global_store_dwordx4 v[174:175], v[168:171], off offset:256
	s_waitcnt vmcnt(15)
	v_cvt_f32_ubyte0_e32 v160, v204
	v_cvt_f32_ubyte1_e32 v161, v204
	v_cvt_f32_ubyte2_e32 v162, v204
	v_cvt_f32_ubyte3_e32 v163, v204
	v_cvt_f32_ubyte0_e32 v164, v205
	v_cvt_f32_ubyte1_e32 v165, v205
	v_cvt_f32_ubyte2_e32 v166, v205
	v_cvt_f32_ubyte3_e32 v167, v205
	v_mul_f32_e32 v160, 0x3b808081, v160
	v_mul_f32_e32 v161, 0x3b808081, v161
	v_mul_f32_e32 v162, 0x3b808081, v162
	v_mul_f32_e32 v163, 0x3b808081, v163
	v_mul_f32_e32 v164, 0x3b808081, v164
	v_mul_f32_e32 v165, 0x3b808081, v165
	v_mul_f32_e32 v166, 0x3b808081, v166
	v_mul_f32_e32 v167, 0x3b808081, v167
	v_max_f32_e32 v160, 0xda24260, v160
	v_max_f32_e32 v161, 0xda24260, v161
	v_max_f32_e32 v162, 0xda24260, v162
	v_max_f32_e32 v163, 0xda24260, v163
	v_max_f32_e32 v164, 0xda24260, v164
	v_max_f32_e32 v165, 0xda24260, v165
	v_max_f32_e32 v166, 0xda24260, v166
	v_max_f32_e32 v167, 0xda24260, v167
	v_mul_f32_e32 v160, v50, v160
	v_mul_f32_e32 v161, v51, v161
	v_mul_f32_e32 v162, v52, v162
	v_mul_f32_e32 v163, v53, v163
	v_mul_f32_e32 v164, v46, v164
	v_mul_f32_e32 v165, v47, v165
	v_mul_f32_e32 v166, v48, v166
	v_mul_f32_e32 v167, v49, v167
	v_cvt_pk_bf16_f32 v168, v160, v161
	v_cvt_pk_bf16_f32 v169, v162, v163
	v_cvt_pk_bf16_f32 v170, v164, v165
	v_cvt_pk_bf16_f32 v171, v166, v167
	v_add_co_u32_e32 v174, vcc, 0x8000, v174
	s_nop 1
	v_addc_co_u32_e32 v175, vcc, 0, v175, vcc
	global_store_dwordx4 v[174:175], v[168:171], off
	s_waitcnt vmcnt(15)
	v_cvt_f32_ubyte0_e32 v160, v206
	v_cvt_f32_ubyte1_e32 v161, v206
	v_cvt_f32_ubyte2_e32 v162, v206
	v_cvt_f32_ubyte3_e32 v163, v206
	v_cvt_f32_ubyte0_e32 v164, v207
	v_cvt_f32_ubyte1_e32 v165, v207
	v_cvt_f32_ubyte2_e32 v166, v207
	v_cvt_f32_ubyte3_e32 v167, v207
	v_mul_f32_e32 v160, 0x3b808081, v160
	v_mul_f32_e32 v161, 0x3b808081, v161
	v_mul_f32_e32 v162, 0x3b808081, v162
	v_mul_f32_e32 v163, 0x3b808081, v163
	v_mul_f32_e32 v164, 0x3b808081, v164
	v_mul_f32_e32 v165, 0x3b808081, v165
	v_mul_f32_e32 v166, 0x3b808081, v166
	v_mul_f32_e32 v167, 0x3b808081, v167
	v_max_f32_e32 v160, 0xda24260, v160
	v_max_f32_e32 v161, 0xda24260, v161
	v_max_f32_e32 v162, 0xda24260, v162
	v_max_f32_e32 v163, 0xda24260, v163
	v_max_f32_e32 v164, 0xda24260, v164
	v_max_f32_e32 v165, 0xda24260, v165
	v_max_f32_e32 v166, 0xda24260, v166
	v_max_f32_e32 v167, 0xda24260, v167
	v_mul_f32_e32 v160, v18, v160
	v_mul_f32_e32 v161, v19, v161
	v_mul_f32_e32 v162, v20, v162
	v_mul_f32_e32 v163, v21, v163
	v_mul_f32_e32 v164, v14, v164
	v_mul_f32_e32 v165, v15, v165
	v_mul_f32_e32 v166, v16, v166
	v_mul_f32_e32 v167, v17, v167
	v_cvt_pk_bf16_f32 v168, v160, v161
	v_cvt_pk_bf16_f32 v169, v162, v163
	v_cvt_pk_bf16_f32 v170, v164, v165
	v_cvt_pk_bf16_f32 v171, v166, v167
	global_store_dwordx4 v[174:175], v[168:171], off offset:256
	s_waitcnt vmcnt(15)
	v_cvt_f32_ubyte0_e32 v160, v208
	v_cvt_f32_ubyte1_e32 v161, v208
	v_cvt_f32_ubyte2_e32 v162, v208
	v_cvt_f32_ubyte3_e32 v163, v208
	v_cvt_f32_ubyte0_e32 v164, v209
	v_cvt_f32_ubyte1_e32 v165, v209
	v_cvt_f32_ubyte2_e32 v166, v209
	v_cvt_f32_ubyte3_e32 v167, v209
	v_mul_f32_e32 v160, 0x3b808081, v160
	v_mul_f32_e32 v161, 0x3b808081, v161
	v_mul_f32_e32 v162, 0x3b808081, v162
	v_mul_f32_e32 v163, 0x3b808081, v163
	v_mul_f32_e32 v164, 0x3b808081, v164
	v_mul_f32_e32 v165, 0x3b808081, v165
	v_mul_f32_e32 v166, 0x3b808081, v166
	v_mul_f32_e32 v167, 0x3b808081, v167
	v_max_f32_e32 v160, 0xda24260, v160
	v_max_f32_e32 v161, 0xda24260, v161
	v_max_f32_e32 v162, 0xda24260, v162
	v_max_f32_e32 v163, 0xda24260, v163
	v_max_f32_e32 v164, 0xda24260, v164
	v_max_f32_e32 v165, 0xda24260, v165
	v_max_f32_e32 v166, 0xda24260, v166
	v_max_f32_e32 v167, 0xda24260, v167
	v_mul_f32_e32 v160, v42, v160
	v_mul_f32_e32 v161, v43, v161
	v_mul_f32_e32 v162, v44, v162
	v_mul_f32_e32 v163, v45, v163
	v_mul_f32_e32 v164, v38, v164
	v_mul_f32_e32 v165, v39, v165
	v_mul_f32_e32 v166, v40, v166
	v_mul_f32_e32 v167, v41, v167
	v_cvt_pk_bf16_f32 v168, v160, v161
	v_cvt_pk_bf16_f32 v169, v162, v163
	v_cvt_pk_bf16_f32 v170, v164, v165
	v_cvt_pk_bf16_f32 v171, v166, v167
	v_add_co_u32_e32 v174, vcc, 0x8000, v174
	s_nop 1
	v_addc_co_u32_e32 v175, vcc, 0, v175, vcc
	global_store_dwordx4 v[174:175], v[168:171], off
	s_waitcnt vmcnt(15)
	v_cvt_f32_ubyte0_e32 v160, v210
	v_cvt_f32_ubyte1_e32 v161, v210
	v_cvt_f32_ubyte2_e32 v162, v210
	v_cvt_f32_ubyte3_e32 v163, v210
	v_cvt_f32_ubyte0_e32 v164, v211
	v_cvt_f32_ubyte1_e32 v165, v211
	v_cvt_f32_ubyte2_e32 v166, v211
	v_cvt_f32_ubyte3_e32 v167, v211
	v_mul_f32_e32 v160, 0x3b808081, v160
	v_mul_f32_e32 v161, 0x3b808081, v161
	v_mul_f32_e32 v162, 0x3b808081, v162
	v_mul_f32_e32 v163, 0x3b808081, v163
	v_mul_f32_e32 v164, 0x3b808081, v164
	v_mul_f32_e32 v165, 0x3b808081, v165
	v_mul_f32_e32 v166, 0x3b808081, v166
	v_mul_f32_e32 v167, 0x3b808081, v167
	v_max_f32_e32 v160, 0xda24260, v160
	v_max_f32_e32 v161, 0xda24260, v161
	v_max_f32_e32 v162, 0xda24260, v162
	v_max_f32_e32 v163, 0xda24260, v163
	v_max_f32_e32 v164, 0xda24260, v164
	v_max_f32_e32 v165, 0xda24260, v165
	v_max_f32_e32 v166, 0xda24260, v166
	v_max_f32_e32 v167, 0xda24260, v167
	v_mul_f32_e32 v160, v10, v160
	v_mul_f32_e32 v161, v11, v161
	v_mul_f32_e32 v162, v12, v162
	v_mul_f32_e32 v163, v13, v163
	v_mul_f32_e32 v164, v6, v164
	v_mul_f32_e32 v165, v7, v165
	v_mul_f32_e32 v166, v8, v166
	v_mul_f32_e32 v167, v9, v167
	v_cvt_pk_bf16_f32 v168, v160, v161
	v_cvt_pk_bf16_f32 v169, v162, v163
	v_cvt_pk_bf16_f32 v170, v164, v165
	v_cvt_pk_bf16_f32 v171, v166, v167
	global_store_dwordx4 v[174:175], v[168:171], off offset:256
	s_mov_b64 s[6:7], 0
.Lp6_done:
	s_andn2_b64 vcc, exec, s[4:5]
	s_mov_b64 s[4:5], -1
	s_cbranch_vccnz .LBB0_1485
.LBB0_1561:
	s_and_b64 vcc, exec, s[6:7]
	s_cbranch_vccnz .LBB0_1563
	v_mov_b32_e32 v4, v2
	v_mov_b32_e32 v5, v2
	v_mov_b32_e32 v3, v2
	v_mov_b64_e32 v[8:9], v[4:5]
	v_mov_b64_e32 v[12:13], v[4:5]
	v_mov_b64_e32 v[16:17], v[4:5]
	v_mov_b64_e32 v[20:21], v[4:5]
	v_mov_b64_e32 v[24:25], v[4:5]
	v_mov_b64_e32 v[28:29], v[4:5]
	v_mov_b64_e32 v[32:33], v[4:5]
	v_mov_b64_e32 v[36:37], v[4:5]
	v_mov_b64_e32 v[40:41], v[4:5]
	v_mov_b64_e32 v[44:45], v[4:5]
	v_mov_b64_e32 v[48:49], v[4:5]
	v_mov_b64_e32 v[52:53], v[4:5]
	v_mov_b64_e32 v[56:57], v[4:5]
	v_mov_b64_e32 v[60:61], v[4:5]
	v_mov_b64_e32 v[64:65], v[4:5]
	v_mov_b64_e32 v[68:69], v[4:5]
	v_mov_b64_e32 v[72:73], v[4:5]
	v_mov_b64_e32 v[76:77], v[4:5]
	v_mov_b64_e32 v[80:81], v[4:5]
	v_mov_b64_e32 v[84:85], v[4:5]
	v_mov_b64_e32 v[88:89], v[4:5]
	v_mov_b64_e32 v[92:93], v[4:5]
	v_mov_b64_e32 v[96:97], v[4:5]
	v_mov_b64_e32 v[100:101], v[4:5]
	v_mov_b64_e32 v[104:105], v[4:5]
	v_mov_b64_e32 v[108:109], v[4:5]
	v_mov_b64_e32 v[112:113], v[4:5]
	v_mov_b64_e32 v[116:117], v[4:5]
	v_mov_b64_e32 v[120:121], v[4:5]
	v_mov_b64_e32 v[124:125], v[4:5]
	v_mov_b64_e32 v[128:129], v[4:5]
	v_mov_b64_e32 v[132:133], v[4:5]
	v_mov_b64_e32 v[6:7], v[2:3]
	v_mov_b64_e32 v[10:11], v[2:3]
	v_mov_b64_e32 v[14:15], v[2:3]
	v_mov_b64_e32 v[18:19], v[2:3]
	v_mov_b64_e32 v[22:23], v[2:3]
	v_mov_b64_e32 v[26:27], v[2:3]
	v_mov_b64_e32 v[30:31], v[2:3]
	v_mov_b64_e32 v[34:35], v[2:3]
	v_mov_b64_e32 v[38:39], v[2:3]
	v_mov_b64_e32 v[42:43], v[2:3]
	v_mov_b64_e32 v[46:47], v[2:3]
	v_mov_b64_e32 v[50:51], v[2:3]
	v_mov_b64_e32 v[54:55], v[2:3]
	v_mov_b64_e32 v[58:59], v[2:3]
	v_mov_b64_e32 v[62:63], v[2:3]
	v_mov_b64_e32 v[66:67], v[2:3]
	v_mov_b64_e32 v[70:71], v[2:3]
	v_mov_b64_e32 v[74:75], v[2:3]
	v_mov_b64_e32 v[78:79], v[2:3]
	v_mov_b64_e32 v[82:83], v[2:3]
	v_mov_b64_e32 v[86:87], v[2:3]
	v_mov_b64_e32 v[90:91], v[2:3]
	v_mov_b64_e32 v[94:95], v[2:3]
	v_mov_b64_e32 v[98:99], v[2:3]
	v_mov_b64_e32 v[102:103], v[2:3]
	v_mov_b64_e32 v[106:107], v[2:3]
	v_mov_b64_e32 v[110:111], v[2:3]
	v_mov_b64_e32 v[114:115], v[2:3]
	v_mov_b64_e32 v[118:119], v[2:3]
	v_mov_b64_e32 v[122:123], v[2:3]
	v_mov_b64_e32 v[126:127], v[2:3]
	v_mov_b64_e32 v[130:131], v[2:3]
